# vI_xnt
# speedup vs baseline: 1.0454x; 1.0454x over previous
.LBB1_4:
	s_or_b64 exec, exec, s[2:3]
	s_load_dwordx2 s[12:13], s[0:1], 0x0
	s_mov_b64 s[0:1], src_shared_base
	s_cmp_lg_u32 0, -1
	s_cselect_b32 s0, s1, 0
	s_cselect_b32 s1, 0, 0
	v_mov_b32_e32 v2, s1
	v_mov_b32_e32 v3, s0
	s_waitcnt lgkmcnt(0)
	s_barrier
	flat_load_dword v2, v[2:3] sc0 sc1
	s_waitcnt vmcnt(0)
	s_movk_i32 s2, 0xff
	v_cmp_lt_u32_e32 vcc, s2, v0
	v_lshlrev_b32_e32 v130, 4, v0
	v_lshrrev_b32_e32 v3, 1, v0
	v_bfe_u32 v202, v0, 5, 1
	v_and_b32_e32 v1, 3, v0
	v_and_b32_e32 v4, 64, v130
	v_and_b32_e32 v3, 12, v3
	v_and_b32_e32 v5, 0x1df0, v130
	v_mul_u32_u24_e32 v6, 0x820, v202
	v_or3_b32 v1, v1, v4, v3
	v_lshl_or_b32 v3, v202, 13, v5
	v_lshl_add_u32 v195, v1, 4, v6
	s_mov_b32 s1, 0
	s_movk_i32 s0, 0x820
	v_add_u32_e32 v1, 0, v195
	v_add_u32_e32 v194, 0, v3
	s_waitcnt lgkmcnt(0)
	s_barrier
	v_readfirstlane_b32 s14, v2
	s_ashr_i32 s2, s14, 1
	s_and_b32 s3, s14, 4
	s_and_b32 s2, s2, -8
	s_lshl_b32 s6, s14, 5
	s_or_b32 s2, s2, s3
	s_and_b32 s28, s6, 0x60
	s_ashr_i32 s33, s2, 2
	s_add_i32 s2, s33, s28
	s_ashr_i32 s3, s2, 31
	s_lshl_b64 s[20:21], s[2:3], 7
	s_bfe_u32 s29, s14, 0x10003
	v_lshrrev_b32_e32 v1, 6, v0
	v_and_b32_e32 v240, 31, v0
	v_bfe_u32 v241, v0, 5, 1
	v_readfirstlane_b32 s34, v1
	s_lshl_b32 s35, s20, 12
	s_add_u32 s40, s12, s35
	s_addc_u32 s41, s13, 0
	s_add_u32 s42, s40, 0x10000
	s_addc_u32 s43, s41, 0
	s_add_u32 s44, s42, 0x10000
	s_addc_u32 s45, s43, 0
	s_add_u32 s46, s44, 0x10000
	s_addc_u32 s47, s45, 0
	s_add_u32 s48, s46, 0x10000
	s_addc_u32 s49, s47, 0
	s_add_u32 s50, s48, 0x10000
	s_addc_u32 s51, s49, 0
	s_add_u32 s52, s50, 0x10000
	s_addc_u32 s53, s51, 0
	s_add_u32 s54, s52, 0x10000
	s_addc_u32 s55, s53, 0
	s_lshl_b32 s35, s29, 20
	s_add_u32 s56, s10, s35
	s_addc_u32 s57, s11, 0
	s_lshl_b32 s35, s34, 10
	v_lshlrev_b32_e32 v1, 4, v240
	v_lshl_add_u32 v1, v241, 13, v1
	v_add_u32_e32 v239, s35, v1
	v_bfe_u32 v1, v240, 2, 1
	v_and_b32_e32 v242, 3, v240
	v_lshrrev_b32_e32 v243, 3, v240
	v_lshl_add_u32 v242, v243, 2, v242
	v_lshl_add_u32 v1, v1, 6, v242
	v_mul_u32_u24_e32 v1, 0x110, v1
	v_lshl_add_u32 v236, v241, 4, v1
	v_lshrrev_b32_e32 v1, 5, v0
	v_lshlrev_b32_e32 v242, 12, v1
	v_lshl_add_u32 v238, v240, 4, v242
	v_mul_u32_u24_e32 v242, 0x110, v1
	v_lshl_add_u32 v237, v240, 3, v242
	s_lshl_b32 s35, s29, 9
	v_and_b32_e32 v1, 0x1c0, v0
	v_or3_b32 v1, s35, v1, v240
	v_lshlrev_b32_e32 v1, 2, v1
	global_load_dword v244, v1, s[8:9]
	global_load_dword v245, v1, s[8:9] offset:128
	global_load_dwordx4 v[204:207], v238, s[40:41] nt
	global_load_dwordx4 v[208:211], v238, s[42:43] nt
	global_load_dwordx4 v[212:215], v238, s[44:45] nt
	global_load_dwordx4 v[216:219], v238, s[46:47] nt
	global_load_dwordx4 v[220:223], v238, s[48:49] nt
	global_load_dwordx4 v[224:227], v238, s[50:51] nt
	global_load_dwordx4 v[228:231], v238, s[52:53] nt
	global_load_dwordx4 v[232:235], v238, s[54:55] nt
	global_load_dwordx4 v[146:149], v239, s[56:57]
	global_load_dwordx4 v[150:153], v239, s[56:57] offset:512
	s_add_u32 s56, s56, 0x4000
	s_addc_u32 s57, s57, 0
	global_load_dwordx4 v[154:157], v239, s[56:57]
	global_load_dwordx4 v[158:161], v239, s[56:57] offset:512
	s_add_u32 s56, s56, 0x4000
	s_addc_u32 s57, s57, 0
	global_load_dwordx4 v[162:165], v239, s[56:57]
	global_load_dwordx4 v[166:169], v239, s[56:57] offset:512
	s_add_u32 s56, s56, 0x4000
	s_addc_u32 s57, s57, 0
	global_load_dwordx4 v[170:173], v239, s[56:57]
	global_load_dwordx4 v[174:177], v239, s[56:57] offset:512
	s_add_u32 s56, s56, 0x4000
	s_addc_u32 s57, s57, 0
	global_load_dwordx4 v[178:181], v239, s[56:57]
	global_load_dwordx4 v[182:185], v239, s[56:57] offset:512
	s_add_u32 s56, s56, 0x4000
	s_addc_u32 s57, s57, 0
	s_waitcnt vmcnt(18)
	s_mov_b32 s38, 0x41a00000
	s_mov_b32 s58, 0

.Lsp_skip:
	s_or_b64 exec, exec, s[36:37]
	v_mov_b32_e32 v244, v245
	v_mov_b32_e32 v245, v187
	s_add_u32 s58, s58, 1
	s_cmp_lt_u32 s58, 2
	s_cbranch_scc1 .Lsp_loop
	s_waitcnt vmcnt(17)
	v_cvt_pk_f16_f32 v204, v204, v205
	v_cvt_pk_f16_f32 v205, v206, v207
	ds_write_b64 v237, v[204:205]
	s_waitcnt vmcnt(16)
	v_cvt_pk_f16_f32 v208, v208, v209
	v_cvt_pk_f16_f32 v209, v210, v211
	ds_write_b64 v237, v[208:209] offset:4352
	s_waitcnt vmcnt(15)
	v_cvt_pk_f16_f32 v212, v212, v213
	v_cvt_pk_f16_f32 v213, v214, v215
	ds_write_b64 v237, v[212:213] offset:8704
	s_waitcnt vmcnt(14)
	v_cvt_pk_f16_f32 v216, v216, v217
	v_cvt_pk_f16_f32 v217, v218, v219
	ds_write_b64 v237, v[216:217] offset:13056
	s_waitcnt vmcnt(13)
	v_cvt_pk_f16_f32 v220, v220, v221
	v_cvt_pk_f16_f32 v221, v222, v223
	ds_write_b64 v237, v[220:221] offset:17408
	s_waitcnt vmcnt(12)
	v_cvt_pk_f16_f32 v224, v224, v225
	v_cvt_pk_f16_f32 v225, v226, v227
	ds_write_b64 v237, v[224:225] offset:21760
	s_waitcnt vmcnt(11)
	v_cvt_pk_f16_f32 v228, v228, v229
	v_cvt_pk_f16_f32 v229, v230, v231
	ds_write_b64 v237, v[228:229] offset:26112
	s_waitcnt vmcnt(10)
	v_cvt_pk_f16_f32 v232, v232, v233
	v_cvt_pk_f16_f32 v233, v234, v235
	ds_write_b64 v237, v[232:233] offset:30464
	global_load_dwordx4 v[204:207], v238, s[40:41] offset:512 nt
	global_load_dwordx4 v[208:211], v238, s[42:43] offset:512 nt
	global_load_dwordx4 v[212:215], v238, s[44:45] offset:512 nt
	global_load_dwordx4 v[216:219], v238, s[46:47] offset:512 nt
	global_load_dwordx4 v[220:223], v238, s[48:49] offset:512 nt
	global_load_dwordx4 v[224:227], v238, s[50:51] offset:512 nt
	global_load_dwordx4 v[228:231], v238, s[52:53] offset:512 nt
	global_load_dwordx4 v[232:235], v238, s[54:55] offset:512 nt
	s_waitcnt lgkmcnt(0)
	s_barrier
	ds_read_b128 v[130:133], v236
	ds_read_b128 v[134:137], v236 offset:4352
	ds_read_b128 v[138:141], v236 offset:8704
	ds_read_b128 v[142:145], v236 offset:13056
	s_waitcnt vmcnt(16)
	s_waitcnt lgkmcnt(3)
	v_mfma_f32_32x32x16_f16 v[82:97], v[130:133], v[146:149], 0
	v_mfma_f32_32x32x16_f16 v[50:65], v[130:133], v[150:153], 0
	ds_read_b128 v[130:133], v236 offset:32
	s_waitcnt lgkmcnt(3)
	v_mfma_f32_32x32x16_f16 v[114:129], v[134:137], v[146:149], 0
	v_mfma_f32_32x32x16_f16 v[34:49], v[134:137], v[150:153], 0
	ds_read_b128 v[134:137], v236 offset:4384
	s_waitcnt lgkmcnt(3)
	v_mfma_f32_32x32x16_f16 v[98:113], v[138:141], v[146:149], 0
	v_mfma_f32_32x32x16_f16 v[18:33], v[138:141], v[150:153], 0
	ds_read_b128 v[138:141], v236 offset:8736
	s_waitcnt lgkmcnt(3)
	v_mfma_f32_32x32x16_f16 v[66:81], v[142:145], v[146:149], 0
	v_mfma_f32_32x32x16_f16 v[2:17], v[142:145], v[150:153], 0
	ds_read_b128 v[142:145], v236 offset:13088
	global_load_dwordx4 v[146:149], v239, s[56:57]
	global_load_dwordx4 v[150:153], v239, s[56:57] offset:512
	s_add_u32 s56, s56, 0x4000
	s_addc_u32 s57, s57, 0
	s_waitcnt vmcnt(16)
	s_waitcnt lgkmcnt(3)
	v_mfma_f32_32x32x16_f16 v[82:97], v[130:133], v[154:157], v[82:97]
	v_mfma_f32_32x32x16_f16 v[50:65], v[130:133], v[158:161], v[50:65]
	ds_read_b128 v[130:133], v236 offset:64
	s_waitcnt lgkmcnt(3)
	v_mfma_f32_32x32x16_f16 v[114:129], v[134:137], v[154:157], v[114:129]
	v_mfma_f32_32x32x16_f16 v[34:49], v[134:137], v[158:161], v[34:49]
	ds_read_b128 v[134:137], v236 offset:4416
	s_waitcnt lgkmcnt(3)
	v_mfma_f32_32x32x16_f16 v[98:113], v[138:141], v[154:157], v[98:113]
	v_mfma_f32_32x32x16_f16 v[18:33], v[138:141], v[158:161], v[18:33]
	ds_read_b128 v[138:141], v236 offset:8768
	s_waitcnt lgkmcnt(3)
	v_mfma_f32_32x32x16_f16 v[66:81], v[142:145], v[154:157], v[66:81]
	v_mfma_f32_32x32x16_f16 v[2:17], v[142:145], v[158:161], v[2:17]
	ds_read_b128 v[142:145], v236 offset:13120
	global_load_dwordx4 v[154:157], v239, s[56:57]
	global_load_dwordx4 v[158:161], v239, s[56:57] offset:512
	s_add_u32 s56, s56, 0x4000
	s_addc_u32 s57, s57, 0
	s_waitcnt vmcnt(16)
	s_waitcnt lgkmcnt(3)
	v_mfma_f32_32x32x16_f16 v[82:97], v[130:133], v[162:165], v[82:97]
	v_mfma_f32_32x32x16_f16 v[50:65], v[130:133], v[166:169], v[50:65]
	ds_read_b128 v[130:133], v236 offset:96
	s_waitcnt lgkmcnt(3)
	v_mfma_f32_32x32x16_f16 v[114:129], v[134:137], v[162:165], v[114:129]
	v_mfma_f32_32x32x16_f16 v[34:49], v[134:137], v[166:169], v[34:49]
	ds_read_b128 v[134:137], v236 offset:4448
	s_waitcnt lgkmcnt(3)
	v_mfma_f32_32x32x16_f16 v[98:113], v[138:141], v[162:165], v[98:113]
	v_mfma_f32_32x32x16_f16 v[18:33], v[138:141], v[166:169], v[18:33]
	ds_read_b128 v[138:141], v236 offset:8800
	s_waitcnt lgkmcnt(3)
	v_mfma_f32_32x32x16_f16 v[66:81], v[142:145], v[162:165], v[66:81]
	v_mfma_f32_32x32x16_f16 v[2:17], v[142:145], v[166:169], v[2:17]
	ds_read_b128 v[142:145], v236 offset:13152
	global_load_dwordx4 v[162:165], v239, s[56:57]
	global_load_dwordx4 v[166:169], v239, s[56:57] offset:512
	s_add_u32 s56, s56, 0x4000
	s_addc_u32 s57, s57, 0
	s_waitcnt vmcnt(16)
	s_waitcnt lgkmcnt(3)
	v_mfma_f32_32x32x16_f16 v[82:97], v[130:133], v[170:173], v[82:97]
	v_mfma_f32_32x32x16_f16 v[50:65], v[130:133], v[174:177], v[50:65]
	ds_read_b128 v[130:133], v236 offset:128
	s_waitcnt lgkmcnt(3)
	v_mfma_f32_32x32x16_f16 v[114:129], v[134:137], v[170:173], v[114:129]
	v_mfma_f32_32x32x16_f16 v[34:49], v[134:137], v[174:177], v[34:49]
	ds_read_b128 v[134:137], v236 offset:4480
	s_waitcnt lgkmcnt(3)
	v_mfma_f32_32x32x16_f16 v[98:113], v[138:141], v[170:173], v[98:113]
	v_mfma_f32_32x32x16_f16 v[18:33], v[138:141], v[174:177], v[18:33]
	ds_read_b128 v[138:141], v236 offset:8832
	s_waitcnt lgkmcnt(3)
	v_mfma_f32_32x32x16_f16 v[66:81], v[142:145], v[170:173], v[66:81]
	v_mfma_f32_32x32x16_f16 v[2:17], v[142:145], v[174:177], v[2:17]
	ds_read_b128 v[142:145], v236 offset:13184
	global_load_dwordx4 v[170:173], v239, s[56:57]
	global_load_dwordx4 v[174:177], v239, s[56:57] offset:512
	s_add_u32 s56, s56, 0x4000
	s_addc_u32 s57, s57, 0
	s_waitcnt vmcnt(16)
	s_waitcnt lgkmcnt(3)
	v_mfma_f32_32x32x16_f16 v[82:97], v[130:133], v[178:181], v[82:97]
	v_mfma_f32_32x32x16_f16 v[50:65], v[130:133], v[182:185], v[50:65]
	ds_read_b128 v[130:133], v236 offset:160
	s_waitcnt lgkmcnt(3)
	v_mfma_f32_32x32x16_f16 v[114:129], v[134:137], v[178:181], v[114:129]
	v_mfma_f32_32x32x16_f16 v[34:49], v[134:137], v[182:185], v[34:49]
	ds_read_b128 v[134:137], v236 offset:4512
	s_waitcnt lgkmcnt(3)
	v_mfma_f32_32x32x16_f16 v[98:113], v[138:141], v[178:181], v[98:113]
	v_mfma_f32_32x32x16_f16 v[18:33], v[138:141], v[182:185], v[18:33]
	ds_read_b128 v[138:141], v236 offset:8864
	s_waitcnt lgkmcnt(3)
	v_mfma_f32_32x32x16_f16 v[66:81], v[142:145], v[178:181], v[66:81]
	v_mfma_f32_32x32x16_f16 v[2:17], v[142:145], v[182:185], v[2:17]
	ds_read_b128 v[142:145], v236 offset:13216
	global_load_dwordx4 v[178:181], v239, s[56:57]
	global_load_dwordx4 v[182:185], v239, s[56:57] offset:512
	s_add_u32 s56, s56, 0x4000
	s_addc_u32 s57, s57, 0
	s_waitcnt vmcnt(8)
	s_waitcnt lgkmcnt(3)
	v_mfma_f32_32x32x16_f16 v[82:97], v[130:133], v[146:149], v[82:97]
	v_mfma_f32_32x32x16_f16 v[50:65], v[130:133], v[150:153], v[50:65]
	ds_read_b128 v[130:133], v236 offset:192
	s_waitcnt lgkmcnt(3)
	v_mfma_f32_32x32x16_f16 v[114:129], v[134:137], v[146:149], v[114:129]
	v_mfma_f32_32x32x16_f16 v[34:49], v[134:137], v[150:153], v[34:49]
	ds_read_b128 v[134:137], v236 offset:4544
	s_waitcnt lgkmcnt(3)
	v_mfma_f32_32x32x16_f16 v[98:113], v[138:141], v[146:149], v[98:113]
	v_mfma_f32_32x32x16_f16 v[18:33], v[138:141], v[150:153], v[18:33]
	ds_read_b128 v[138:141], v236 offset:8896
	s_waitcnt lgkmcnt(3)
	v_mfma_f32_32x32x16_f16 v[66:81], v[142:145], v[146:149], v[66:81]
	v_mfma_f32_32x32x16_f16 v[2:17], v[142:145], v[150:153], v[2:17]
	ds_read_b128 v[142:145], v236 offset:13248
	global_load_dwordx4 v[146:149], v239, s[56:57]
	global_load_dwordx4 v[150:153], v239, s[56:57] offset:512
	s_add_u32 s56, s56, 0x4000
	s_addc_u32 s57, s57, 0
	s_waitcnt vmcnt(19)
	v_cvt_pk_f16_f32 v204, v204, v205
	v_cvt_pk_f16_f32 v205, v206, v207
	ds_write_b64 v237, v[204:205] offset:34816
	s_waitcnt vmcnt(18)
	v_cvt_pk_f16_f32 v208, v208, v209
	v_cvt_pk_f16_f32 v209, v210, v211
	ds_write_b64 v237, v[208:209] offset:39168
	s_waitcnt vmcnt(17)
	v_cvt_pk_f16_f32 v212, v212, v213
	v_cvt_pk_f16_f32 v213, v214, v215
	ds_write_b64 v237, v[212:213] offset:43520
	s_waitcnt vmcnt(16)
	v_cvt_pk_f16_f32 v216, v216, v217
	v_cvt_pk_f16_f32 v217, v218, v219
	ds_write_b64 v237, v[216:217] offset:47872
	s_waitcnt vmcnt(15)
	v_cvt_pk_f16_f32 v220, v220, v221
	v_cvt_pk_f16_f32 v221, v222, v223
	ds_write_b64 v237, v[220:221] offset:52224
	s_waitcnt vmcnt(14)
	v_cvt_pk_f16_f32 v224, v224, v225
	v_cvt_pk_f16_f32 v225, v226, v227
	ds_write_b64 v237, v[224:225] offset:56576
	s_waitcnt vmcnt(13)
	v_cvt_pk_f16_f32 v228, v228, v229
	v_cvt_pk_f16_f32 v229, v230, v231
	ds_write_b64 v237, v[228:229] offset:60928
	s_waitcnt vmcnt(12)
	v_cvt_pk_f16_f32 v232, v232, v233
	v_cvt_pk_f16_f32 v233, v234, v235
	ds_write_b64 v237, v[232:233] offset:65280
	global_load_dwordx4 v[204:207], v238, s[40:41] offset:1024 nt
	global_load_dwordx4 v[208:211], v238, s[42:43] offset:1024 nt
	global_load_dwordx4 v[212:215], v238, s[44:45] offset:1024 nt
	global_load_dwordx4 v[216:219], v238, s[46:47] offset:1024 nt
	global_load_dwordx4 v[220:223], v238, s[48:49] offset:1024 nt
	global_load_dwordx4 v[224:227], v238, s[50:51] offset:1024 nt
	global_load_dwordx4 v[228:231], v238, s[52:53] offset:1024 nt
	global_load_dwordx4 v[232:235], v238, s[54:55] offset:1024 nt
	s_waitcnt vmcnt(16)
	s_waitcnt lgkmcnt(11)
	v_mfma_f32_32x32x16_f16 v[82:97], v[130:133], v[154:157], v[82:97]
	v_mfma_f32_32x32x16_f16 v[50:65], v[130:133], v[158:161], v[50:65]
	ds_read_b128 v[130:133], v236 offset:224
	s_waitcnt lgkmcnt(11)
	v_mfma_f32_32x32x16_f16 v[114:129], v[134:137], v[154:157], v[114:129]
	v_mfma_f32_32x32x16_f16 v[34:49], v[134:137], v[158:161], v[34:49]
	ds_read_b128 v[134:137], v236 offset:4576
	s_waitcnt lgkmcnt(11)
	v_mfma_f32_32x32x16_f16 v[98:113], v[138:141], v[154:157], v[98:113]
	v_mfma_f32_32x32x16_f16 v[18:33], v[138:141], v[158:161], v[18:33]
	ds_read_b128 v[138:141], v236 offset:8928
	s_waitcnt lgkmcnt(11)
	v_mfma_f32_32x32x16_f16 v[66:81], v[142:145], v[154:157], v[66:81]
	v_mfma_f32_32x32x16_f16 v[2:17], v[142:145], v[158:161], v[2:17]
	ds_read_b128 v[142:145], v236 offset:13280
	global_load_dwordx4 v[154:157], v239, s[56:57]
	global_load_dwordx4 v[158:161], v239, s[56:57] offset:512
	s_add_u32 s56, s56, 0x4000
	s_addc_u32 s57, s57, 0
	s_waitcnt vmcnt(16)
	s_waitcnt lgkmcnt(3)
	v_mfma_f32_32x32x16_f16 v[82:97], v[130:133], v[162:165], v[82:97]
	v_mfma_f32_32x32x16_f16 v[50:65], v[130:133], v[166:169], v[50:65]
	s_waitcnt lgkmcnt(2)
	v_mfma_f32_32x32x16_f16 v[114:129], v[134:137], v[162:165], v[114:129]
	v_mfma_f32_32x32x16_f16 v[34:49], v[134:137], v[166:169], v[34:49]
	s_waitcnt lgkmcnt(1)
	v_mfma_f32_32x32x16_f16 v[98:113], v[138:141], v[162:165], v[98:113]
	v_mfma_f32_32x32x16_f16 v[18:33], v[138:141], v[166:169], v[18:33]
	s_waitcnt lgkmcnt(0)
	v_mfma_f32_32x32x16_f16 v[66:81], v[142:145], v[162:165], v[66:81]
	v_mfma_f32_32x32x16_f16 v[2:17], v[142:145], v[166:169], v[2:17]
	global_load_dwordx4 v[162:165], v239, s[56:57]
	global_load_dwordx4 v[166:169], v239, s[56:57] offset:512
	s_add_u32 s56, s56, 0x4000
	s_addc_u32 s57, s57, 0
	s_waitcnt lgkmcnt(0)
	s_barrier
	ds_read_b128 v[130:133], v236 offset:34816
	ds_read_b128 v[134:137], v236 offset:39168
	ds_read_b128 v[138:141], v236 offset:43520
	ds_read_b128 v[142:145], v236 offset:47872
	s_waitcnt vmcnt(16)
	s_waitcnt lgkmcnt(3)
	v_mfma_f32_32x32x16_f16 v[82:97], v[130:133], v[170:173], v[82:97]
	v_mfma_f32_32x32x16_f16 v[50:65], v[130:133], v[174:177], v[50:65]
	ds_read_b128 v[130:133], v236 offset:34848
	s_waitcnt lgkmcnt(3)
	v_mfma_f32_32x32x16_f16 v[114:129], v[134:137], v[170:173], v[114:129]
	v_mfma_f32_32x32x16_f16 v[34:49], v[134:137], v[174:177], v[34:49]
	ds_read_b128 v[134:137], v236 offset:39200
	s_waitcnt lgkmcnt(3)
	v_mfma_f32_32x32x16_f16 v[98:113], v[138:141], v[170:173], v[98:113]
	v_mfma_f32_32x32x16_f16 v[18:33], v[138:141], v[174:177], v[18:33]
	ds_read_b128 v[138:141], v236 offset:43552
	s_waitcnt lgkmcnt(3)
	v_mfma_f32_32x32x16_f16 v[66:81], v[142:145], v[170:173], v[66:81]
	v_mfma_f32_32x32x16_f16 v[2:17], v[142:145], v[174:177], v[2:17]
	ds_read_b128 v[142:145], v236 offset:47904
	global_load_dwordx4 v[170:173], v239, s[56:57]
	global_load_dwordx4 v[174:177], v239, s[56:57] offset:512
	s_add_u32 s56, s56, 0x4000
	s_addc_u32 s57, s57, 0
	s_waitcnt vmcnt(16)
	s_waitcnt lgkmcnt(3)
	v_mfma_f32_32x32x16_f16 v[82:97], v[130:133], v[178:181], v[82:97]
	v_mfma_f32_32x32x16_f16 v[50:65], v[130:133], v[182:185], v[50:65]
	ds_read_b128 v[130:133], v236 offset:34880
	s_waitcnt lgkmcnt(3)
	v_mfma_f32_32x32x16_f16 v[114:129], v[134:137], v[178:181], v[114:129]
	v_mfma_f32_32x32x16_f16 v[34:49], v[134:137], v[182:185], v[34:49]
	ds_read_b128 v[134:137], v236 offset:39232
	s_waitcnt lgkmcnt(3)
	v_mfma_f32_32x32x16_f16 v[98:113], v[138:141], v[178:181], v[98:113]
	v_mfma_f32_32x32x16_f16 v[18:33], v[138:141], v[182:185], v[18:33]
	ds_read_b128 v[138:141], v236 offset:43584
	s_waitcnt lgkmcnt(3)
	v_mfma_f32_32x32x16_f16 v[66:81], v[142:145], v[178:181], v[66:81]
	v_mfma_f32_32x32x16_f16 v[2:17], v[142:145], v[182:185], v[2:17]
	ds_read_b128 v[142:145], v236 offset:47936
	global_load_dwordx4 v[178:181], v239, s[56:57]
	global_load_dwordx4 v[182:185], v239, s[56:57] offset:512
	s_add_u32 s56, s56, 0x4000
	s_addc_u32 s57, s57, 0
	s_waitcnt vmcnt(16)
	s_waitcnt lgkmcnt(3)
	v_mfma_f32_32x32x16_f16 v[82:97], v[130:133], v[146:149], v[82:97]
	v_mfma_f32_32x32x16_f16 v[50:65], v[130:133], v[150:153], v[50:65]
	ds_read_b128 v[130:133], v236 offset:34912
	s_waitcnt lgkmcnt(3)
	v_mfma_f32_32x32x16_f16 v[114:129], v[134:137], v[146:149], v[114:129]
	v_mfma_f32_32x32x16_f16 v[34:49], v[134:137], v[150:153], v[34:49]
	ds_read_b128 v[134:137], v236 offset:39264
	s_waitcnt lgkmcnt(3)
	v_mfma_f32_32x32x16_f16 v[98:113], v[138:141], v[146:149], v[98:113]
	v_mfma_f32_32x32x16_f16 v[18:33], v[138:141], v[150:153], v[18:33]
	ds_read_b128 v[138:141], v236 offset:43616
	s_waitcnt lgkmcnt(3)
	v_mfma_f32_32x32x16_f16 v[66:81], v[142:145], v[146:149], v[66:81]
	v_mfma_f32_32x32x16_f16 v[2:17], v[142:145], v[150:153], v[2:17]
	ds_read_b128 v[142:145], v236 offset:47968
	global_load_dwordx4 v[146:149], v239, s[56:57]
	global_load_dwordx4 v[150:153], v239, s[56:57] offset:512
	s_add_u32 s56, s56, 0x4000
	s_addc_u32 s57, s57, 0
	s_waitcnt vmcnt(8)
	s_waitcnt lgkmcnt(3)
	v_mfma_f32_32x32x16_f16 v[82:97], v[130:133], v[154:157], v[82:97]
	v_mfma_f32_32x32x16_f16 v[50:65], v[130:133], v[158:161], v[50:65]
	ds_read_b128 v[130:133], v236 offset:34944
	s_waitcnt lgkmcnt(3)
	v_mfma_f32_32x32x16_f16 v[114:129], v[134:137], v[154:157], v[114:129]
	v_mfma_f32_32x32x16_f16 v[34:49], v[134:137], v[158:161], v[34:49]
	ds_read_b128 v[134:137], v236 offset:39296
	s_waitcnt lgkmcnt(3)
	v_mfma_f32_32x32x16_f16 v[98:113], v[138:141], v[154:157], v[98:113]
	v_mfma_f32_32x32x16_f16 v[18:33], v[138:141], v[158:161], v[18:33]
	ds_read_b128 v[138:141], v236 offset:43648
	s_waitcnt lgkmcnt(3)
	v_mfma_f32_32x32x16_f16 v[66:81], v[142:145], v[154:157], v[66:81]
	v_mfma_f32_32x32x16_f16 v[2:17], v[142:145], v[158:161], v[2:17]
	ds_read_b128 v[142:145], v236 offset:48000
	global_load_dwordx4 v[154:157], v239, s[56:57]
	global_load_dwordx4 v[158:161], v239, s[56:57] offset:512
	s_add_u32 s56, s56, 0x4000
	s_addc_u32 s57, s57, 0
	s_waitcnt vmcnt(8)
	s_waitcnt lgkmcnt(3)
	v_mfma_f32_32x32x16_f16 v[82:97], v[130:133], v[162:165], v[82:97]
	v_mfma_f32_32x32x16_f16 v[50:65], v[130:133], v[166:169], v[50:65]
	ds_read_b128 v[130:133], v236 offset:34976
	s_waitcnt lgkmcnt(3)
	v_mfma_f32_32x32x16_f16 v[114:129], v[134:137], v[162:165], v[114:129]
	v_mfma_f32_32x32x16_f16 v[34:49], v[134:137], v[166:169], v[34:49]
	ds_read_b128 v[134:137], v236 offset:39328
	s_waitcnt lgkmcnt(3)
	v_mfma_f32_32x32x16_f16 v[98:113], v[138:141], v[162:165], v[98:113]
	v_mfma_f32_32x32x16_f16 v[18:33], v[138:141], v[166:169], v[18:33]
	ds_read_b128 v[138:141], v236 offset:43680
	s_waitcnt lgkmcnt(3)
	v_mfma_f32_32x32x16_f16 v[66:81], v[142:145], v[162:165], v[66:81]
	v_mfma_f32_32x32x16_f16 v[2:17], v[142:145], v[166:169], v[2:17]
	ds_read_b128 v[142:145], v236 offset:48032
	global_load_dwordx4 v[162:165], v239, s[56:57]
	global_load_dwordx4 v[166:169], v239, s[56:57] offset:512
	s_add_u32 s56, s56, 0x4000
	s_addc_u32 s57, s57, 0
	s_waitcnt vmcnt(8)
	s_waitcnt lgkmcnt(3)
	v_mfma_f32_32x32x16_f16 v[82:97], v[130:133], v[170:173], v[82:97]
	v_mfma_f32_32x32x16_f16 v[50:65], v[130:133], v[174:177], v[50:65]
	ds_read_b128 v[130:133], v236 offset:35008
	s_waitcnt lgkmcnt(3)
	v_mfma_f32_32x32x16_f16 v[114:129], v[134:137], v[170:173], v[114:129]
	v_mfma_f32_32x32x16_f16 v[34:49], v[134:137], v[174:177], v[34:49]
	ds_read_b128 v[134:137], v236 offset:39360
	s_waitcnt lgkmcnt(3)
	v_mfma_f32_32x32x16_f16 v[98:113], v[138:141], v[170:173], v[98:113]
	v_mfma_f32_32x32x16_f16 v[18:33], v[138:141], v[174:177], v[18:33]
	ds_read_b128 v[138:141], v236 offset:43712
	s_waitcnt lgkmcnt(3)
	v_mfma_f32_32x32x16_f16 v[66:81], v[142:145], v[170:173], v[66:81]
	v_mfma_f32_32x32x16_f16 v[2:17], v[142:145], v[174:177], v[2:17]
	ds_read_b128 v[142:145], v236 offset:48064
	global_load_dwordx4 v[170:173], v239, s[56:57]
	global_load_dwordx4 v[174:177], v239, s[56:57] offset:512
	s_add_u32 s56, s56, 0x4000
	s_addc_u32 s57, s57, 0
	s_waitcnt vmcnt(23)
	v_cvt_pk_f16_f32 v204, v204, v205
	v_cvt_pk_f16_f32 v205, v206, v207
	ds_write_b64 v237, v[204:205]
	s_waitcnt vmcnt(22)
	v_cvt_pk_f16_f32 v208, v208, v209
	v_cvt_pk_f16_f32 v209, v210, v211
	ds_write_b64 v237, v[208:209] offset:4352
	s_waitcnt vmcnt(21)
	v_cvt_pk_f16_f32 v212, v212, v213
	v_cvt_pk_f16_f32 v213, v214, v215
	ds_write_b64 v237, v[212:213] offset:8704
	s_waitcnt vmcnt(20)
	v_cvt_pk_f16_f32 v216, v216, v217
	v_cvt_pk_f16_f32 v217, v218, v219
	ds_write_b64 v237, v[216:217] offset:13056
	s_waitcnt vmcnt(19)
	v_cvt_pk_f16_f32 v220, v220, v221
	v_cvt_pk_f16_f32 v221, v222, v223
	ds_write_b64 v237, v[220:221] offset:17408
	s_waitcnt vmcnt(18)
	v_cvt_pk_f16_f32 v224, v224, v225
	v_cvt_pk_f16_f32 v225, v226, v227
	ds_write_b64 v237, v[224:225] offset:21760
	s_waitcnt vmcnt(17)
	v_cvt_pk_f16_f32 v228, v228, v229
	v_cvt_pk_f16_f32 v229, v230, v231
	ds_write_b64 v237, v[228:229] offset:26112
	s_waitcnt vmcnt(16)
	v_cvt_pk_f16_f32 v232, v232, v233
	v_cvt_pk_f16_f32 v233, v234, v235
	ds_write_b64 v237, v[232:233] offset:30464
	global_load_dwordx4 v[204:207], v238, s[40:41] offset:1536 nt
	global_load_dwordx4 v[208:211], v238, s[42:43] offset:1536 nt
	global_load_dwordx4 v[212:215], v238, s[44:45] offset:1536 nt
	global_load_dwordx4 v[216:219], v238, s[46:47] offset:1536 nt
	global_load_dwordx4 v[220:223], v238, s[48:49] offset:1536 nt
	global_load_dwordx4 v[224:227], v238, s[50:51] offset:1536 nt
	global_load_dwordx4 v[228:231], v238, s[52:53] offset:1536 nt
	global_load_dwordx4 v[232:235], v238, s[54:55] offset:1536 nt
	s_waitcnt vmcnt(16)
	s_waitcnt lgkmcnt(11)
	v_mfma_f32_32x32x16_f16 v[82:97], v[130:133], v[178:181], v[82:97]
	v_mfma_f32_32x32x16_f16 v[50:65], v[130:133], v[182:185], v[50:65]
	ds_read_b128 v[130:133], v236 offset:35040
	s_waitcnt lgkmcnt(11)
	v_mfma_f32_32x32x16_f16 v[114:129], v[134:137], v[178:181], v[114:129]
	v_mfma_f32_32x32x16_f16 v[34:49], v[134:137], v[182:185], v[34:49]
	ds_read_b128 v[134:137], v236 offset:39392
	s_waitcnt lgkmcnt(11)
	v_mfma_f32_32x32x16_f16 v[98:113], v[138:141], v[178:181], v[98:113]
	v_mfma_f32_32x32x16_f16 v[18:33], v[138:141], v[182:185], v[18:33]
	ds_read_b128 v[138:141], v236 offset:43744
	s_waitcnt lgkmcnt(11)
	v_mfma_f32_32x32x16_f16 v[66:81], v[142:145], v[178:181], v[66:81]
	v_mfma_f32_32x32x16_f16 v[2:17], v[142:145], v[182:185], v[2:17]
	ds_read_b128 v[142:145], v236 offset:48096
	global_load_dwordx4 v[178:181], v239, s[56:57]
	global_load_dwordx4 v[182:185], v239, s[56:57] offset:512
	s_add_u32 s56, s56, 0x4000
	s_addc_u32 s57, s57, 0
	s_waitcnt vmcnt(16)
	s_waitcnt lgkmcnt(3)
	v_mfma_f32_32x32x16_f16 v[82:97], v[130:133], v[146:149], v[82:97]
	v_mfma_f32_32x32x16_f16 v[50:65], v[130:133], v[150:153], v[50:65]
	s_waitcnt lgkmcnt(2)
	v_mfma_f32_32x32x16_f16 v[114:129], v[134:137], v[146:149], v[114:129]
	v_mfma_f32_32x32x16_f16 v[34:49], v[134:137], v[150:153], v[34:49]
	s_waitcnt lgkmcnt(1)
	v_mfma_f32_32x32x16_f16 v[98:113], v[138:141], v[146:149], v[98:113]
	v_mfma_f32_32x32x16_f16 v[18:33], v[138:141], v[150:153], v[18:33]
	s_waitcnt lgkmcnt(0)
	v_mfma_f32_32x32x16_f16 v[66:81], v[142:145], v[146:149], v[66:81]
	v_mfma_f32_32x32x16_f16 v[2:17], v[142:145], v[150:153], v[2:17]
	global_load_dwordx4 v[146:149], v239, s[56:57]
	global_load_dwordx4 v[150:153], v239, s[56:57] offset:512
	s_add_u32 s56, s56, 0x4000
	s_addc_u32 s57, s57, 0
	s_waitcnt lgkmcnt(0)
	s_barrier
	ds_read_b128 v[130:133], v236
	ds_read_b128 v[134:137], v236 offset:4352
	ds_read_b128 v[138:141], v236 offset:8704
	ds_read_b128 v[142:145], v236 offset:13056
	s_waitcnt vmcnt(16)
	s_waitcnt lgkmcnt(3)
	v_mfma_f32_32x32x16_f16 v[82:97], v[130:133], v[154:157], v[82:97]
	v_mfma_f32_32x32x16_f16 v[50:65], v[130:133], v[158:161], v[50:65]
	ds_read_b128 v[130:133], v236 offset:32
	s_waitcnt lgkmcnt(3)
	v_mfma_f32_32x32x16_f16 v[114:129], v[134:137], v[154:157], v[114:129]
	v_mfma_f32_32x32x16_f16 v[34:49], v[134:137], v[158:161], v[34:49]
	ds_read_b128 v[134:137], v236 offset:4384
	s_waitcnt lgkmcnt(3)
	v_mfma_f32_32x32x16_f16 v[98:113], v[138:141], v[154:157], v[98:113]
	v_mfma_f32_32x32x16_f16 v[18:33], v[138:141], v[158:161], v[18:33]
	ds_read_b128 v[138:141], v236 offset:8736
	s_waitcnt lgkmcnt(3)
	v_mfma_f32_32x32x16_f16 v[66:81], v[142:145], v[154:157], v[66:81]
	v_mfma_f32_32x32x16_f16 v[2:17], v[142:145], v[158:161], v[2:17]
	ds_read_b128 v[142:145], v236 offset:13088
	global_load_dwordx4 v[154:157], v239, s[56:57]
	global_load_dwordx4 v[158:161], v239, s[56:57] offset:512
	s_add_u32 s56, s56, 0x4000
	s_addc_u32 s57, s57, 0
	s_waitcnt vmcnt(16)
	s_waitcnt lgkmcnt(3)
	v_mfma_f32_32x32x16_f16 v[82:97], v[130:133], v[162:165], v[82:97]
	v_mfma_f32_32x32x16_f16 v[50:65], v[130:133], v[166:169], v[50:65]
	ds_read_b128 v[130:133], v236 offset:64
	s_waitcnt lgkmcnt(3)
	v_mfma_f32_32x32x16_f16 v[114:129], v[134:137], v[162:165], v[114:129]
	v_mfma_f32_32x32x16_f16 v[34:49], v[134:137], v[166:169], v[34:49]
	ds_read_b128 v[134:137], v236 offset:4416
	s_waitcnt lgkmcnt(3)
	v_mfma_f32_32x32x16_f16 v[98:113], v[138:141], v[162:165], v[98:113]
	v_mfma_f32_32x32x16_f16 v[18:33], v[138:141], v[166:169], v[18:33]
	ds_read_b128 v[138:141], v236 offset:8768
	s_waitcnt lgkmcnt(3)
	v_mfma_f32_32x32x16_f16 v[66:81], v[142:145], v[162:165], v[66:81]
	v_mfma_f32_32x32x16_f16 v[2:17], v[142:145], v[166:169], v[2:17]
	ds_read_b128 v[142:145], v236 offset:13120
	global_load_dwordx4 v[162:165], v239, s[56:57]
	global_load_dwordx4 v[166:169], v239, s[56:57] offset:512
	s_add_u32 s56, s56, 0x4000
	s_addc_u32 s57, s57, 0
	s_waitcnt vmcnt(16)
	s_waitcnt lgkmcnt(3)
	v_mfma_f32_32x32x16_f16 v[82:97], v[130:133], v[170:173], v[82:97]
	v_mfma_f32_32x32x16_f16 v[50:65], v[130:133], v[174:177], v[50:65]
	ds_read_b128 v[130:133], v236 offset:96
	s_waitcnt lgkmcnt(3)
	v_mfma_f32_32x32x16_f16 v[114:129], v[134:137], v[170:173], v[114:129]
	v_mfma_f32_32x32x16_f16 v[34:49], v[134:137], v[174:177], v[34:49]
	ds_read_b128 v[134:137], v236 offset:4448
	s_waitcnt lgkmcnt(3)
	v_mfma_f32_32x32x16_f16 v[98:113], v[138:141], v[170:173], v[98:113]
	v_mfma_f32_32x32x16_f16 v[18:33], v[138:141], v[174:177], v[18:33]
	ds_read_b128 v[138:141], v236 offset:8800
	s_waitcnt lgkmcnt(3)
	v_mfma_f32_32x32x16_f16 v[66:81], v[142:145], v[170:173], v[66:81]
	v_mfma_f32_32x32x16_f16 v[2:17], v[142:145], v[174:177], v[2:17]
	ds_read_b128 v[142:145], v236 offset:13152
	global_load_dwordx4 v[170:173], v239, s[56:57]
	global_load_dwordx4 v[174:177], v239, s[56:57] offset:512
	s_add_u32 s56, s56, 0x4000
	s_addc_u32 s57, s57, 0
	s_waitcnt vmcnt(8)
	s_waitcnt lgkmcnt(3)
	v_mfma_f32_32x32x16_f16 v[82:97], v[130:133], v[178:181], v[82:97]
	v_mfma_f32_32x32x16_f16 v[50:65], v[130:133], v[182:185], v[50:65]
	ds_read_b128 v[130:133], v236 offset:128
	s_waitcnt lgkmcnt(3)
	v_mfma_f32_32x32x16_f16 v[114:129], v[134:137], v[178:181], v[114:129]
	v_mfma_f32_32x32x16_f16 v[34:49], v[134:137], v[182:185], v[34:49]
	ds_read_b128 v[134:137], v236 offset:4480
	s_waitcnt lgkmcnt(3)
	v_mfma_f32_32x32x16_f16 v[98:113], v[138:141], v[178:181], v[98:113]
	v_mfma_f32_32x32x16_f16 v[18:33], v[138:141], v[182:185], v[18:33]
	ds_read_b128 v[138:141], v236 offset:8832
	s_waitcnt lgkmcnt(3)
	v_mfma_f32_32x32x16_f16 v[66:81], v[142:145], v[178:181], v[66:81]
	v_mfma_f32_32x32x16_f16 v[2:17], v[142:145], v[182:185], v[2:17]
	ds_read_b128 v[142:145], v236 offset:13184
	global_load_dwordx4 v[178:181], v239, s[56:57]
	global_load_dwordx4 v[182:185], v239, s[56:57] offset:512
	s_add_u32 s56, s56, 0x4000
	s_addc_u32 s57, s57, 0
	s_waitcnt vmcnt(8)
	s_waitcnt lgkmcnt(3)
	v_mfma_f32_32x32x16_f16 v[82:97], v[130:133], v[146:149], v[82:97]
	v_mfma_f32_32x32x16_f16 v[50:65], v[130:133], v[150:153], v[50:65]
	ds_read_b128 v[130:133], v236 offset:160
	s_waitcnt lgkmcnt(3)
	v_mfma_f32_32x32x16_f16 v[114:129], v[134:137], v[146:149], v[114:129]
	v_mfma_f32_32x32x16_f16 v[34:49], v[134:137], v[150:153], v[34:49]
	ds_read_b128 v[134:137], v236 offset:4512
	s_waitcnt lgkmcnt(3)
	v_mfma_f32_32x32x16_f16 v[98:113], v[138:141], v[146:149], v[98:113]
	v_mfma_f32_32x32x16_f16 v[18:33], v[138:141], v[150:153], v[18:33]
	ds_read_b128 v[138:141], v236 offset:8864
	s_waitcnt lgkmcnt(3)
	v_mfma_f32_32x32x16_f16 v[66:81], v[142:145], v[146:149], v[66:81]
	v_mfma_f32_32x32x16_f16 v[2:17], v[142:145], v[150:153], v[2:17]
	ds_read_b128 v[142:145], v236 offset:13216
	global_load_dwordx4 v[146:149], v239, s[56:57]
	global_load_dwordx4 v[150:153], v239, s[56:57] offset:512
	s_add_u32 s56, s56, 0x4000
	s_addc_u32 s57, s57, 0
	s_waitcnt vmcnt(8)
	s_waitcnt lgkmcnt(3)
	v_mfma_f32_32x32x16_f16 v[82:97], v[130:133], v[154:157], v[82:97]
	v_mfma_f32_32x32x16_f16 v[50:65], v[130:133], v[158:161], v[50:65]
	ds_read_b128 v[130:133], v236 offset:192
	s_waitcnt lgkmcnt(3)
	v_mfma_f32_32x32x16_f16 v[114:129], v[134:137], v[154:157], v[114:129]
	v_mfma_f32_32x32x16_f16 v[34:49], v[134:137], v[158:161], v[34:49]
	ds_read_b128 v[134:137], v236 offset:4544
	s_waitcnt lgkmcnt(3)
	v_mfma_f32_32x32x16_f16 v[98:113], v[138:141], v[154:157], v[98:113]
	v_mfma_f32_32x32x16_f16 v[18:33], v[138:141], v[158:161], v[18:33]
	ds_read_b128 v[138:141], v236 offset:8896
	s_waitcnt lgkmcnt(3)
	v_mfma_f32_32x32x16_f16 v[66:81], v[142:145], v[154:157], v[66:81]
	v_mfma_f32_32x32x16_f16 v[2:17], v[142:145], v[158:161], v[2:17]
	ds_read_b128 v[142:145], v236 offset:13248
	global_load_dwordx4 v[154:157], v239, s[56:57]
	global_load_dwordx4 v[158:161], v239, s[56:57] offset:512
	s_add_u32 s56, s56, 0x4000
	s_addc_u32 s57, s57, 0
	s_waitcnt vmcnt(23)
	v_cvt_pk_f16_f32 v204, v204, v205
	v_cvt_pk_f16_f32 v205, v206, v207
	ds_write_b64 v237, v[204:205] offset:34816
	s_waitcnt vmcnt(22)
	v_cvt_pk_f16_f32 v208, v208, v209
	v_cvt_pk_f16_f32 v209, v210, v211
	ds_write_b64 v237, v[208:209] offset:39168
	s_waitcnt vmcnt(21)
	v_cvt_pk_f16_f32 v212, v212, v213
	v_cvt_pk_f16_f32 v213, v214, v215
	ds_write_b64 v237, v[212:213] offset:43520
	s_waitcnt vmcnt(20)
	v_cvt_pk_f16_f32 v216, v216, v217
	v_cvt_pk_f16_f32 v217, v218, v219
	ds_write_b64 v237, v[216:217] offset:47872
	s_waitcnt vmcnt(19)
	v_cvt_pk_f16_f32 v220, v220, v221
	v_cvt_pk_f16_f32 v221, v222, v223
	ds_write_b64 v237, v[220:221] offset:52224
	s_waitcnt vmcnt(18)
	v_cvt_pk_f16_f32 v224, v224, v225
	v_cvt_pk_f16_f32 v225, v226, v227
	ds_write_b64 v237, v[224:225] offset:56576
	s_waitcnt vmcnt(17)
	v_cvt_pk_f16_f32 v228, v228, v229
	v_cvt_pk_f16_f32 v229, v230, v231
	ds_write_b64 v237, v[228:229] offset:60928
	s_waitcnt vmcnt(16)
	v_cvt_pk_f16_f32 v232, v232, v233
	v_cvt_pk_f16_f32 v233, v234, v235
	ds_write_b64 v237, v[232:233] offset:65280
	global_load_dwordx4 v[204:207], v238, s[40:41] offset:2048 nt
	global_load_dwordx4 v[208:211], v238, s[42:43] offset:2048 nt
	global_load_dwordx4 v[212:215], v238, s[44:45] offset:2048 nt
	global_load_dwordx4 v[216:219], v238, s[46:47] offset:2048 nt
	global_load_dwordx4 v[220:223], v238, s[48:49] offset:2048 nt
	global_load_dwordx4 v[224:227], v238, s[50:51] offset:2048 nt
	global_load_dwordx4 v[228:231], v238, s[52:53] offset:2048 nt
	global_load_dwordx4 v[232:235], v238, s[54:55] offset:2048 nt
	s_waitcnt vmcnt(16)
	s_waitcnt lgkmcnt(11)
	v_mfma_f32_32x32x16_f16 v[82:97], v[130:133], v[162:165], v[82:97]
	v_mfma_f32_32x32x16_f16 v[50:65], v[130:133], v[166:169], v[50:65]
	ds_read_b128 v[130:133], v236 offset:224
	s_waitcnt lgkmcnt(11)
	v_mfma_f32_32x32x16_f16 v[114:129], v[134:137], v[162:165], v[114:129]
	v_mfma_f32_32x32x16_f16 v[34:49], v[134:137], v[166:169], v[34:49]
	ds_read_b128 v[134:137], v236 offset:4576
	s_waitcnt lgkmcnt(11)
	v_mfma_f32_32x32x16_f16 v[98:113], v[138:141], v[162:165], v[98:113]
	v_mfma_f32_32x32x16_f16 v[18:33], v[138:141], v[166:169], v[18:33]
	ds_read_b128 v[138:141], v236 offset:8928
	s_waitcnt lgkmcnt(11)
	v_mfma_f32_32x32x16_f16 v[66:81], v[142:145], v[162:165], v[66:81]
	v_mfma_f32_32x32x16_f16 v[2:17], v[142:145], v[166:169], v[2:17]
	ds_read_b128 v[142:145], v236 offset:13280
	global_load_dwordx4 v[162:165], v239, s[56:57]
	global_load_dwordx4 v[166:169], v239, s[56:57] offset:512
	s_add_u32 s56, s56, 0x4000
	s_addc_u32 s57, s57, 0
	s_waitcnt vmcnt(16)
	s_waitcnt lgkmcnt(3)
	v_mfma_f32_32x32x16_f16 v[82:97], v[130:133], v[170:173], v[82:97]
	v_mfma_f32_32x32x16_f16 v[50:65], v[130:133], v[174:177], v[50:65]
	s_waitcnt lgkmcnt(2)
	v_mfma_f32_32x32x16_f16 v[114:129], v[134:137], v[170:173], v[114:129]
	v_mfma_f32_32x32x16_f16 v[34:49], v[134:137], v[174:177], v[34:49]
	s_waitcnt lgkmcnt(1)
	v_mfma_f32_32x32x16_f16 v[98:113], v[138:141], v[170:173], v[98:113]
	v_mfma_f32_32x32x16_f16 v[18:33], v[138:141], v[174:177], v[18:33]
	s_waitcnt lgkmcnt(0)
	v_mfma_f32_32x32x16_f16 v[66:81], v[142:145], v[170:173], v[66:81]
	v_mfma_f32_32x32x16_f16 v[2:17], v[142:145], v[174:177], v[2:17]
	global_load_dwordx4 v[170:173], v239, s[56:57]
	global_load_dwordx4 v[174:177], v239, s[56:57] offset:512
	s_add_u32 s56, s56, 0x4000
	s_addc_u32 s57, s57, 0
	s_waitcnt lgkmcnt(0)
	s_barrier
	ds_read_b128 v[130:133], v236 offset:34816
	ds_read_b128 v[134:137], v236 offset:39168
	ds_read_b128 v[138:141], v236 offset:43520
	ds_read_b128 v[142:145], v236 offset:47872
	s_waitcnt vmcnt(16)
	s_waitcnt lgkmcnt(3)
	v_mfma_f32_32x32x16_f16 v[82:97], v[130:133], v[178:181], v[82:97]
	v_mfma_f32_32x32x16_f16 v[50:65], v[130:133], v[182:185], v[50:65]
	ds_read_b128 v[130:133], v236 offset:34848
	s_waitcnt lgkmcnt(3)
	v_mfma_f32_32x32x16_f16 v[114:129], v[134:137], v[178:181], v[114:129]
	v_mfma_f32_32x32x16_f16 v[34:49], v[134:137], v[182:185], v[34:49]
	ds_read_b128 v[134:137], v236 offset:39200
	s_waitcnt lgkmcnt(3)
	v_mfma_f32_32x32x16_f16 v[98:113], v[138:141], v[178:181], v[98:113]
	v_mfma_f32_32x32x16_f16 v[18:33], v[138:141], v[182:185], v[18:33]
	ds_read_b128 v[138:141], v236 offset:43552
	s_waitcnt lgkmcnt(3)
	v_mfma_f32_32x32x16_f16 v[66:81], v[142:145], v[178:181], v[66:81]
	v_mfma_f32_32x32x16_f16 v[2:17], v[142:145], v[182:185], v[2:17]
	ds_read_b128 v[142:145], v236 offset:47904
	global_load_dwordx4 v[178:181], v239, s[56:57]
	global_load_dwordx4 v[182:185], v239, s[56:57] offset:512
	s_add_u32 s56, s56, 0x4000
	s_addc_u32 s57, s57, 0
	s_waitcnt vmcnt(16)
	s_waitcnt lgkmcnt(3)
	v_mfma_f32_32x32x16_f16 v[82:97], v[130:133], v[146:149], v[82:97]
	v_mfma_f32_32x32x16_f16 v[50:65], v[130:133], v[150:153], v[50:65]
	ds_read_b128 v[130:133], v236 offset:34880
	s_waitcnt lgkmcnt(3)
	v_mfma_f32_32x32x16_f16 v[114:129], v[134:137], v[146:149], v[114:129]
	v_mfma_f32_32x32x16_f16 v[34:49], v[134:137], v[150:153], v[34:49]
	ds_read_b128 v[134:137], v236 offset:39232
	s_waitcnt lgkmcnt(3)
	v_mfma_f32_32x32x16_f16 v[98:113], v[138:141], v[146:149], v[98:113]
	v_mfma_f32_32x32x16_f16 v[18:33], v[138:141], v[150:153], v[18:33]
	ds_read_b128 v[138:141], v236 offset:43584
	s_waitcnt lgkmcnt(3)
	v_mfma_f32_32x32x16_f16 v[66:81], v[142:145], v[146:149], v[66:81]
	v_mfma_f32_32x32x16_f16 v[2:17], v[142:145], v[150:153], v[2:17]
	ds_read_b128 v[142:145], v236 offset:47936
	global_load_dwordx4 v[146:149], v239, s[56:57]
	global_load_dwordx4 v[150:153], v239, s[56:57] offset:512
	s_add_u32 s56, s56, 0x4000
	s_addc_u32 s57, s57, 0
	s_waitcnt vmcnt(16)
	s_waitcnt lgkmcnt(3)
	v_mfma_f32_32x32x16_f16 v[82:97], v[130:133], v[154:157], v[82:97]
	v_mfma_f32_32x32x16_f16 v[50:65], v[130:133], v[158:161], v[50:65]
	ds_read_b128 v[130:133], v236 offset:34912
	s_waitcnt lgkmcnt(3)
	v_mfma_f32_32x32x16_f16 v[114:129], v[134:137], v[154:157], v[114:129]
	v_mfma_f32_32x32x16_f16 v[34:49], v[134:137], v[158:161], v[34:49]
	ds_read_b128 v[134:137], v236 offset:39264
	s_waitcnt lgkmcnt(3)
	v_mfma_f32_32x32x16_f16 v[98:113], v[138:141], v[154:157], v[98:113]
	v_mfma_f32_32x32x16_f16 v[18:33], v[138:141], v[158:161], v[18:33]
	ds_read_b128 v[138:141], v236 offset:43616
	s_waitcnt lgkmcnt(3)
	v_mfma_f32_32x32x16_f16 v[66:81], v[142:145], v[154:157], v[66:81]
	v_mfma_f32_32x32x16_f16 v[2:17], v[142:145], v[158:161], v[2:17]
	ds_read_b128 v[142:145], v236 offset:47968
	global_load_dwordx4 v[154:157], v239, s[56:57]
	global_load_dwordx4 v[158:161], v239, s[56:57] offset:512
	s_add_u32 s56, s56, 0x4000
	s_addc_u32 s57, s57, 0
	s_waitcnt vmcnt(8)
	s_waitcnt lgkmcnt(3)
	v_mfma_f32_32x32x16_f16 v[82:97], v[130:133], v[162:165], v[82:97]
	v_mfma_f32_32x32x16_f16 v[50:65], v[130:133], v[166:169], v[50:65]
	ds_read_b128 v[130:133], v236 offset:34944
	s_waitcnt lgkmcnt(3)
	v_mfma_f32_32x32x16_f16 v[114:129], v[134:137], v[162:165], v[114:129]
	v_mfma_f32_32x32x16_f16 v[34:49], v[134:137], v[166:169], v[34:49]
	ds_read_b128 v[134:137], v236 offset:39296
	s_waitcnt lgkmcnt(3)
	v_mfma_f32_32x32x16_f16 v[98:113], v[138:141], v[162:165], v[98:113]
	v_mfma_f32_32x32x16_f16 v[18:33], v[138:141], v[166:169], v[18:33]
	ds_read_b128 v[138:141], v236 offset:43648
	s_waitcnt lgkmcnt(3)
	v_mfma_f32_32x32x16_f16 v[66:81], v[142:145], v[162:165], v[66:81]
	v_mfma_f32_32x32x16_f16 v[2:17], v[142:145], v[166:169], v[2:17]
	ds_read_b128 v[142:145], v236 offset:48000
	global_load_dwordx4 v[162:165], v239, s[56:57]
	global_load_dwordx4 v[166:169], v239, s[56:57] offset:512
	s_add_u32 s56, s56, 0x4000
	s_addc_u32 s57, s57, 0
	s_waitcnt vmcnt(8)
	s_waitcnt lgkmcnt(3)
	v_mfma_f32_32x32x16_f16 v[82:97], v[130:133], v[170:173], v[82:97]
	v_mfma_f32_32x32x16_f16 v[50:65], v[130:133], v[174:177], v[50:65]
	ds_read_b128 v[130:133], v236 offset:34976
	s_waitcnt lgkmcnt(3)
	v_mfma_f32_32x32x16_f16 v[114:129], v[134:137], v[170:173], v[114:129]
	v_mfma_f32_32x32x16_f16 v[34:49], v[134:137], v[174:177], v[34:49]
	ds_read_b128 v[134:137], v236 offset:39328
	s_waitcnt lgkmcnt(3)
	v_mfma_f32_32x32x16_f16 v[98:113], v[138:141], v[170:173], v[98:113]
	v_mfma_f32_32x32x16_f16 v[18:33], v[138:141], v[174:177], v[18:33]
	ds_read_b128 v[138:141], v236 offset:43680
	s_waitcnt lgkmcnt(3)
	v_mfma_f32_32x32x16_f16 v[66:81], v[142:145], v[170:173], v[66:81]
	v_mfma_f32_32x32x16_f16 v[2:17], v[142:145], v[174:177], v[2:17]
	ds_read_b128 v[142:145], v236 offset:48032
	global_load_dwordx4 v[170:173], v239, s[56:57]
	global_load_dwordx4 v[174:177], v239, s[56:57] offset:512
	s_add_u32 s56, s56, 0x4000
	s_addc_u32 s57, s57, 0
	s_waitcnt vmcnt(8)
	s_waitcnt lgkmcnt(3)
	v_mfma_f32_32x32x16_f16 v[82:97], v[130:133], v[178:181], v[82:97]
	v_mfma_f32_32x32x16_f16 v[50:65], v[130:133], v[182:185], v[50:65]
	ds_read_b128 v[130:133], v236 offset:35008
	s_waitcnt lgkmcnt(3)
	v_mfma_f32_32x32x16_f16 v[114:129], v[134:137], v[178:181], v[114:129]
	v_mfma_f32_32x32x16_f16 v[34:49], v[134:137], v[182:185], v[34:49]
	ds_read_b128 v[134:137], v236 offset:39360
	s_waitcnt lgkmcnt(3)
	v_mfma_f32_32x32x16_f16 v[98:113], v[138:141], v[178:181], v[98:113]
	v_mfma_f32_32x32x16_f16 v[18:33], v[138:141], v[182:185], v[18:33]
	ds_read_b128 v[138:141], v236 offset:43712
	s_waitcnt lgkmcnt(3)
	v_mfma_f32_32x32x16_f16 v[66:81], v[142:145], v[178:181], v[66:81]
	v_mfma_f32_32x32x16_f16 v[2:17], v[142:145], v[182:185], v[2:17]
	ds_read_b128 v[142:145], v236 offset:48064
	global_load_dwordx4 v[178:181], v239, s[56:57]
	global_load_dwordx4 v[182:185], v239, s[56:57] offset:512
	s_add_u32 s56, s56, 0x4000
	s_addc_u32 s57, s57, 0
	s_waitcnt vmcnt(23)
	v_cvt_pk_f16_f32 v204, v204, v205
	v_cvt_pk_f16_f32 v205, v206, v207
	ds_write_b64 v237, v[204:205]
	s_waitcnt vmcnt(22)
	v_cvt_pk_f16_f32 v208, v208, v209
	v_cvt_pk_f16_f32 v209, v210, v211
	ds_write_b64 v237, v[208:209] offset:4352
	s_waitcnt vmcnt(21)
	v_cvt_pk_f16_f32 v212, v212, v213
	v_cvt_pk_f16_f32 v213, v214, v215
	ds_write_b64 v237, v[212:213] offset:8704
	s_waitcnt vmcnt(20)
	v_cvt_pk_f16_f32 v216, v216, v217
	v_cvt_pk_f16_f32 v217, v218, v219
	ds_write_b64 v237, v[216:217] offset:13056
	s_waitcnt vmcnt(19)
	v_cvt_pk_f16_f32 v220, v220, v221
	v_cvt_pk_f16_f32 v221, v222, v223
	ds_write_b64 v237, v[220:221] offset:17408
	s_waitcnt vmcnt(18)
	v_cvt_pk_f16_f32 v224, v224, v225
	v_cvt_pk_f16_f32 v225, v226, v227
	ds_write_b64 v237, v[224:225] offset:21760
	s_waitcnt vmcnt(17)
	v_cvt_pk_f16_f32 v228, v228, v229
	v_cvt_pk_f16_f32 v229, v230, v231
	ds_write_b64 v237, v[228:229] offset:26112
	s_waitcnt vmcnt(16)
	v_cvt_pk_f16_f32 v232, v232, v233
	v_cvt_pk_f16_f32 v233, v234, v235
	ds_write_b64 v237, v[232:233] offset:30464
	global_load_dwordx4 v[204:207], v238, s[40:41] offset:2560 nt
	global_load_dwordx4 v[208:211], v238, s[42:43] offset:2560 nt
	global_load_dwordx4 v[212:215], v238, s[44:45] offset:2560 nt
	global_load_dwordx4 v[216:219], v238, s[46:47] offset:2560 nt
	global_load_dwordx4 v[220:223], v238, s[48:49] offset:2560 nt
	global_load_dwordx4 v[224:227], v238, s[50:51] offset:2560 nt
	global_load_dwordx4 v[228:231], v238, s[52:53] offset:2560 nt
	global_load_dwordx4 v[232:235], v238, s[54:55] offset:2560 nt
	s_waitcnt vmcnt(16)
	s_waitcnt lgkmcnt(11)
	v_mfma_f32_32x32x16_f16 v[82:97], v[130:133], v[146:149], v[82:97]
	v_mfma_f32_32x32x16_f16 v[50:65], v[130:133], v[150:153], v[50:65]
	ds_read_b128 v[130:133], v236 offset:35040
	s_waitcnt lgkmcnt(11)
	v_mfma_f32_32x32x16_f16 v[114:129], v[134:137], v[146:149], v[114:129]
	v_mfma_f32_32x32x16_f16 v[34:49], v[134:137], v[150:153], v[34:49]
	ds_read_b128 v[134:137], v236 offset:39392
	s_waitcnt lgkmcnt(11)
	v_mfma_f32_32x32x16_f16 v[98:113], v[138:141], v[146:149], v[98:113]
	v_mfma_f32_32x32x16_f16 v[18:33], v[138:141], v[150:153], v[18:33]
	ds_read_b128 v[138:141], v236 offset:43744
	s_waitcnt lgkmcnt(11)
	v_mfma_f32_32x32x16_f16 v[66:81], v[142:145], v[146:149], v[66:81]
	v_mfma_f32_32x32x16_f16 v[2:17], v[142:145], v[150:153], v[2:17]
	ds_read_b128 v[142:145], v236 offset:48096
	global_load_dwordx4 v[146:149], v239, s[56:57]
	global_load_dwordx4 v[150:153], v239, s[56:57] offset:512
	s_add_u32 s56, s56, 0x4000
	s_addc_u32 s57, s57, 0
	s_waitcnt vmcnt(16)
	s_waitcnt lgkmcnt(3)
	v_mfma_f32_32x32x16_f16 v[82:97], v[130:133], v[154:157], v[82:97]
	v_mfma_f32_32x32x16_f16 v[50:65], v[130:133], v[158:161], v[50:65]
	s_waitcnt lgkmcnt(2)
	v_mfma_f32_32x32x16_f16 v[114:129], v[134:137], v[154:157], v[114:129]
	v_mfma_f32_32x32x16_f16 v[34:49], v[134:137], v[158:161], v[34:49]
	s_waitcnt lgkmcnt(1)
	v_mfma_f32_32x32x16_f16 v[98:113], v[138:141], v[154:157], v[98:113]
	v_mfma_f32_32x32x16_f16 v[18:33], v[138:141], v[158:161], v[18:33]
	s_waitcnt lgkmcnt(0)
	v_mfma_f32_32x32x16_f16 v[66:81], v[142:145], v[154:157], v[66:81]
	v_mfma_f32_32x32x16_f16 v[2:17], v[142:145], v[158:161], v[2:17]
	global_load_dwordx4 v[154:157], v239, s[56:57]
	global_load_dwordx4 v[158:161], v239, s[56:57] offset:512
	s_add_u32 s56, s56, 0x4000
	s_addc_u32 s57, s57, 0
	s_waitcnt lgkmcnt(0)
	s_barrier
	ds_read_b128 v[130:133], v236
	ds_read_b128 v[134:137], v236 offset:4352
	ds_read_b128 v[138:141], v236 offset:8704
	ds_read_b128 v[142:145], v236 offset:13056
	s_waitcnt vmcnt(16)
	s_waitcnt lgkmcnt(3)
	v_mfma_f32_32x32x16_f16 v[82:97], v[130:133], v[162:165], v[82:97]
	v_mfma_f32_32x32x16_f16 v[50:65], v[130:133], v[166:169], v[50:65]
	ds_read_b128 v[130:133], v236 offset:32
	s_waitcnt lgkmcnt(3)
	v_mfma_f32_32x32x16_f16 v[114:129], v[134:137], v[162:165], v[114:129]
	v_mfma_f32_32x32x16_f16 v[34:49], v[134:137], v[166:169], v[34:49]
	ds_read_b128 v[134:137], v236 offset:4384
	s_waitcnt lgkmcnt(3)
	v_mfma_f32_32x32x16_f16 v[98:113], v[138:141], v[162:165], v[98:113]
	v_mfma_f32_32x32x16_f16 v[18:33], v[138:141], v[166:169], v[18:33]
	ds_read_b128 v[138:141], v236 offset:8736
	s_waitcnt lgkmcnt(3)
	v_mfma_f32_32x32x16_f16 v[66:81], v[142:145], v[162:165], v[66:81]
	v_mfma_f32_32x32x16_f16 v[2:17], v[142:145], v[166:169], v[2:17]
	ds_read_b128 v[142:145], v236 offset:13088
	global_load_dwordx4 v[162:165], v239, s[56:57]
	global_load_dwordx4 v[166:169], v239, s[56:57] offset:512
	s_add_u32 s56, s56, 0x4000
	s_addc_u32 s57, s57, 0
	s_waitcnt vmcnt(16)
	s_waitcnt lgkmcnt(3)
	v_mfma_f32_32x32x16_f16 v[82:97], v[130:133], v[170:173], v[82:97]
	v_mfma_f32_32x32x16_f16 v[50:65], v[130:133], v[174:177], v[50:65]
	ds_read_b128 v[130:133], v236 offset:64
	s_waitcnt lgkmcnt(3)
	v_mfma_f32_32x32x16_f16 v[114:129], v[134:137], v[170:173], v[114:129]
	v_mfma_f32_32x32x16_f16 v[34:49], v[134:137], v[174:177], v[34:49]
	ds_read_b128 v[134:137], v236 offset:4416
	s_waitcnt lgkmcnt(3)
	v_mfma_f32_32x32x16_f16 v[98:113], v[138:141], v[170:173], v[98:113]
	v_mfma_f32_32x32x16_f16 v[18:33], v[138:141], v[174:177], v[18:33]
	ds_read_b128 v[138:141], v236 offset:8768
	s_waitcnt lgkmcnt(3)
	v_mfma_f32_32x32x16_f16 v[66:81], v[142:145], v[170:173], v[66:81]
	v_mfma_f32_32x32x16_f16 v[2:17], v[142:145], v[174:177], v[2:17]
	ds_read_b128 v[142:145], v236 offset:13120
	global_load_dwordx4 v[170:173], v239, s[56:57]
	global_load_dwordx4 v[174:177], v239, s[56:57] offset:512
	s_add_u32 s56, s56, 0x4000
	s_addc_u32 s57, s57, 0
	s_waitcnt vmcnt(16)
	s_waitcnt lgkmcnt(3)
	v_mfma_f32_32x32x16_f16 v[82:97], v[130:133], v[178:181], v[82:97]
	v_mfma_f32_32x32x16_f16 v[50:65], v[130:133], v[182:185], v[50:65]
	ds_read_b128 v[130:133], v236 offset:96
	s_waitcnt lgkmcnt(3)
	v_mfma_f32_32x32x16_f16 v[114:129], v[134:137], v[178:181], v[114:129]
	v_mfma_f32_32x32x16_f16 v[34:49], v[134:137], v[182:185], v[34:49]
	ds_read_b128 v[134:137], v236 offset:4448
	s_waitcnt lgkmcnt(3)
	v_mfma_f32_32x32x16_f16 v[98:113], v[138:141], v[178:181], v[98:113]
	v_mfma_f32_32x32x16_f16 v[18:33], v[138:141], v[182:185], v[18:33]
	ds_read_b128 v[138:141], v236 offset:8800
	s_waitcnt lgkmcnt(3)
	v_mfma_f32_32x32x16_f16 v[66:81], v[142:145], v[178:181], v[66:81]
	v_mfma_f32_32x32x16_f16 v[2:17], v[142:145], v[182:185], v[2:17]
	ds_read_b128 v[142:145], v236 offset:13152
	global_load_dwordx4 v[178:181], v239, s[56:57]
	global_load_dwordx4 v[182:185], v239, s[56:57] offset:512
	s_add_u32 s56, s56, 0x4000
	s_addc_u32 s57, s57, 0
	s_waitcnt vmcnt(8)
	s_waitcnt lgkmcnt(3)
	v_mfma_f32_32x32x16_f16 v[82:97], v[130:133], v[146:149], v[82:97]
	v_mfma_f32_32x32x16_f16 v[50:65], v[130:133], v[150:153], v[50:65]
	ds_read_b128 v[130:133], v236 offset:128
	s_waitcnt lgkmcnt(3)
	v_mfma_f32_32x32x16_f16 v[114:129], v[134:137], v[146:149], v[114:129]
	v_mfma_f32_32x32x16_f16 v[34:49], v[134:137], v[150:153], v[34:49]
	ds_read_b128 v[134:137], v236 offset:4480
	s_waitcnt lgkmcnt(3)
	v_mfma_f32_32x32x16_f16 v[98:113], v[138:141], v[146:149], v[98:113]
	v_mfma_f32_32x32x16_f16 v[18:33], v[138:141], v[150:153], v[18:33]
	ds_read_b128 v[138:141], v236 offset:8832
	s_waitcnt lgkmcnt(3)
	v_mfma_f32_32x32x16_f16 v[66:81], v[142:145], v[146:149], v[66:81]
	v_mfma_f32_32x32x16_f16 v[2:17], v[142:145], v[150:153], v[2:17]
	ds_read_b128 v[142:145], v236 offset:13184
	global_load_dwordx4 v[146:149], v239, s[56:57]
	global_load_dwordx4 v[150:153], v239, s[56:57] offset:512
	s_add_u32 s56, s56, 0x4000
	s_addc_u32 s57, s57, 0
	s_waitcnt vmcnt(8)
	s_waitcnt lgkmcnt(3)
	v_mfma_f32_32x32x16_f16 v[82:97], v[130:133], v[154:157], v[82:97]
	v_mfma_f32_32x32x16_f16 v[50:65], v[130:133], v[158:161], v[50:65]
	ds_read_b128 v[130:133], v236 offset:160
	s_waitcnt lgkmcnt(3)
	v_mfma_f32_32x32x16_f16 v[114:129], v[134:137], v[154:157], v[114:129]
	v_mfma_f32_32x32x16_f16 v[34:49], v[134:137], v[158:161], v[34:49]
	ds_read_b128 v[134:137], v236 offset:4512
	s_waitcnt lgkmcnt(3)
	v_mfma_f32_32x32x16_f16 v[98:113], v[138:141], v[154:157], v[98:113]
	v_mfma_f32_32x32x16_f16 v[18:33], v[138:141], v[158:161], v[18:33]
	ds_read_b128 v[138:141], v236 offset:8864
	s_waitcnt lgkmcnt(3)
	v_mfma_f32_32x32x16_f16 v[66:81], v[142:145], v[154:157], v[66:81]
	v_mfma_f32_32x32x16_f16 v[2:17], v[142:145], v[158:161], v[2:17]
	ds_read_b128 v[142:145], v236 offset:13216
	global_load_dwordx4 v[154:157], v239, s[56:57]
	global_load_dwordx4 v[158:161], v239, s[56:57] offset:512
	s_add_u32 s56, s56, 0x4000
	s_addc_u32 s57, s57, 0
	s_waitcnt vmcnt(8)
	s_waitcnt lgkmcnt(3)
	v_mfma_f32_32x32x16_f16 v[82:97], v[130:133], v[162:165], v[82:97]
	v_mfma_f32_32x32x16_f16 v[50:65], v[130:133], v[166:169], v[50:65]
	ds_read_b128 v[130:133], v236 offset:192
	s_waitcnt lgkmcnt(3)
	v_mfma_f32_32x32x16_f16 v[114:129], v[134:137], v[162:165], v[114:129]
	v_mfma_f32_32x32x16_f16 v[34:49], v[134:137], v[166:169], v[34:49]
	ds_read_b128 v[134:137], v236 offset:4544
	s_waitcnt lgkmcnt(3)
	v_mfma_f32_32x32x16_f16 v[98:113], v[138:141], v[162:165], v[98:113]
	v_mfma_f32_32x32x16_f16 v[18:33], v[138:141], v[166:169], v[18:33]
	ds_read_b128 v[138:141], v236 offset:8896
	s_waitcnt lgkmcnt(3)
	v_mfma_f32_32x32x16_f16 v[66:81], v[142:145], v[162:165], v[66:81]
	v_mfma_f32_32x32x16_f16 v[2:17], v[142:145], v[166:169], v[2:17]
	ds_read_b128 v[142:145], v236 offset:13248
	global_load_dwordx4 v[162:165], v239, s[56:57]
	global_load_dwordx4 v[166:169], v239, s[56:57] offset:512
	s_add_u32 s56, s56, 0x4000
	s_addc_u32 s57, s57, 0
	s_waitcnt vmcnt(23)
	v_cvt_pk_f16_f32 v204, v204, v205
	v_cvt_pk_f16_f32 v205, v206, v207
	ds_write_b64 v237, v[204:205] offset:34816
	s_waitcnt vmcnt(22)
	v_cvt_pk_f16_f32 v208, v208, v209
	v_cvt_pk_f16_f32 v209, v210, v211
	ds_write_b64 v237, v[208:209] offset:39168
	s_waitcnt vmcnt(21)
	v_cvt_pk_f16_f32 v212, v212, v213
	v_cvt_pk_f16_f32 v213, v214, v215
	ds_write_b64 v237, v[212:213] offset:43520
	s_waitcnt vmcnt(20)
	v_cvt_pk_f16_f32 v216, v216, v217
	v_cvt_pk_f16_f32 v217, v218, v219
	ds_write_b64 v237, v[216:217] offset:47872
	s_waitcnt vmcnt(19)
	v_cvt_pk_f16_f32 v220, v220, v221
	v_cvt_pk_f16_f32 v221, v222, v223
	ds_write_b64 v237, v[220:221] offset:52224
	s_waitcnt vmcnt(18)
	v_cvt_pk_f16_f32 v224, v224, v225
	v_cvt_pk_f16_f32 v225, v226, v227
	ds_write_b64 v237, v[224:225] offset:56576
	s_waitcnt vmcnt(17)
	v_cvt_pk_f16_f32 v228, v228, v229
	v_cvt_pk_f16_f32 v229, v230, v231
	ds_write_b64 v237, v[228:229] offset:60928
	s_waitcnt vmcnt(16)
	v_cvt_pk_f16_f32 v232, v232, v233
	v_cvt_pk_f16_f32 v233, v234, v235
	ds_write_b64 v237, v[232:233] offset:65280
	global_load_dwordx4 v[204:207], v238, s[40:41] offset:3072 nt
	global_load_dwordx4 v[208:211], v238, s[42:43] offset:3072 nt
	global_load_dwordx4 v[212:215], v238, s[44:45] offset:3072 nt
	global_load_dwordx4 v[216:219], v238, s[46:47] offset:3072 nt
	global_load_dwordx4 v[220:223], v238, s[48:49] offset:3072 nt
	global_load_dwordx4 v[224:227], v238, s[50:51] offset:3072 nt
	global_load_dwordx4 v[228:231], v238, s[52:53] offset:3072 nt
	global_load_dwordx4 v[232:235], v238, s[54:55] offset:3072 nt
	s_waitcnt vmcnt(16)
	s_waitcnt lgkmcnt(11)
	v_mfma_f32_32x32x16_f16 v[82:97], v[130:133], v[170:173], v[82:97]
	v_mfma_f32_32x32x16_f16 v[50:65], v[130:133], v[174:177], v[50:65]
	ds_read_b128 v[130:133], v236 offset:224
	s_waitcnt lgkmcnt(11)
	v_mfma_f32_32x32x16_f16 v[114:129], v[134:137], v[170:173], v[114:129]
	v_mfma_f32_32x32x16_f16 v[34:49], v[134:137], v[174:177], v[34:49]
	ds_read_b128 v[134:137], v236 offset:4576
	s_waitcnt lgkmcnt(11)
	v_mfma_f32_32x32x16_f16 v[98:113], v[138:141], v[170:173], v[98:113]
	v_mfma_f32_32x32x16_f16 v[18:33], v[138:141], v[174:177], v[18:33]
	ds_read_b128 v[138:141], v236 offset:8928
	s_waitcnt lgkmcnt(11)
	v_mfma_f32_32x32x16_f16 v[66:81], v[142:145], v[170:173], v[66:81]
	v_mfma_f32_32x32x16_f16 v[2:17], v[142:145], v[174:177], v[2:17]
	ds_read_b128 v[142:145], v236 offset:13280
	global_load_dwordx4 v[170:173], v239, s[56:57]
	global_load_dwordx4 v[174:177], v239, s[56:57] offset:512
	s_add_u32 s56, s56, 0x4000
	s_addc_u32 s57, s57, 0
	s_waitcnt vmcnt(16)
	s_waitcnt lgkmcnt(3)
	v_mfma_f32_32x32x16_f16 v[82:97], v[130:133], v[178:181], v[82:97]
	v_mfma_f32_32x32x16_f16 v[50:65], v[130:133], v[182:185], v[50:65]
	s_waitcnt lgkmcnt(2)
	v_mfma_f32_32x32x16_f16 v[114:129], v[134:137], v[178:181], v[114:129]
	v_mfma_f32_32x32x16_f16 v[34:49], v[134:137], v[182:185], v[34:49]
	s_waitcnt lgkmcnt(1)
	v_mfma_f32_32x32x16_f16 v[98:113], v[138:141], v[178:181], v[98:113]
	v_mfma_f32_32x32x16_f16 v[18:33], v[138:141], v[182:185], v[18:33]
	s_waitcnt lgkmcnt(0)
	v_mfma_f32_32x32x16_f16 v[66:81], v[142:145], v[178:181], v[66:81]
	v_mfma_f32_32x32x16_f16 v[2:17], v[142:145], v[182:185], v[2:17]
	global_load_dwordx4 v[178:181], v239, s[56:57]
	global_load_dwordx4 v[182:185], v239, s[56:57] offset:512
	s_add_u32 s56, s56, 0x4000
	s_addc_u32 s57, s57, 0
	s_waitcnt lgkmcnt(0)
	s_barrier
	ds_read_b128 v[130:133], v236 offset:34816
	ds_read_b128 v[134:137], v236 offset:39168
	ds_read_b128 v[138:141], v236 offset:43520
	ds_read_b128 v[142:145], v236 offset:47872
	s_waitcnt vmcnt(16)
	s_waitcnt lgkmcnt(3)
	v_mfma_f32_32x32x16_f16 v[82:97], v[130:133], v[146:149], v[82:97]
	v_mfma_f32_32x32x16_f16 v[50:65], v[130:133], v[150:153], v[50:65]
	ds_read_b128 v[130:133], v236 offset:34848
	s_waitcnt lgkmcnt(3)
	v_mfma_f32_32x32x16_f16 v[114:129], v[134:137], v[146:149], v[114:129]
	v_mfma_f32_32x32x16_f16 v[34:49], v[134:137], v[150:153], v[34:49]
	ds_read_b128 v[134:137], v236 offset:39200
	s_waitcnt lgkmcnt(3)
	v_mfma_f32_32x32x16_f16 v[98:113], v[138:141], v[146:149], v[98:113]
	v_mfma_f32_32x32x16_f16 v[18:33], v[138:141], v[150:153], v[18:33]
	ds_read_b128 v[138:141], v236 offset:43552
	s_waitcnt lgkmcnt(3)
	v_mfma_f32_32x32x16_f16 v[66:81], v[142:145], v[146:149], v[66:81]
	v_mfma_f32_32x32x16_f16 v[2:17], v[142:145], v[150:153], v[2:17]
	ds_read_b128 v[142:145], v236 offset:47904
	global_load_dwordx4 v[146:149], v239, s[56:57]
	global_load_dwordx4 v[150:153], v239, s[56:57] offset:512
	s_add_u32 s56, s56, 0x4000
	s_addc_u32 s57, s57, 0
	s_waitcnt vmcnt(16)
	s_waitcnt lgkmcnt(3)
	v_mfma_f32_32x32x16_f16 v[82:97], v[130:133], v[154:157], v[82:97]
	v_mfma_f32_32x32x16_f16 v[50:65], v[130:133], v[158:161], v[50:65]
	ds_read_b128 v[130:133], v236 offset:34880
	s_waitcnt lgkmcnt(3)
	v_mfma_f32_32x32x16_f16 v[114:129], v[134:137], v[154:157], v[114:129]
	v_mfma_f32_32x32x16_f16 v[34:49], v[134:137], v[158:161], v[34:49]
	ds_read_b128 v[134:137], v236 offset:39232
	s_waitcnt lgkmcnt(3)
	v_mfma_f32_32x32x16_f16 v[98:113], v[138:141], v[154:157], v[98:113]
	v_mfma_f32_32x32x16_f16 v[18:33], v[138:141], v[158:161], v[18:33]
	ds_read_b128 v[138:141], v236 offset:43584
	s_waitcnt lgkmcnt(3)
	v_mfma_f32_32x32x16_f16 v[66:81], v[142:145], v[154:157], v[66:81]
	v_mfma_f32_32x32x16_f16 v[2:17], v[142:145], v[158:161], v[2:17]
	ds_read_b128 v[142:145], v236 offset:47936
	global_load_dwordx4 v[154:157], v239, s[56:57]
	global_load_dwordx4 v[158:161], v239, s[56:57] offset:512
	s_add_u32 s56, s56, 0x4000
	s_addc_u32 s57, s57, 0
	s_waitcnt vmcnt(16)
	s_waitcnt lgkmcnt(3)
	v_mfma_f32_32x32x16_f16 v[82:97], v[130:133], v[162:165], v[82:97]
	v_mfma_f32_32x32x16_f16 v[50:65], v[130:133], v[166:169], v[50:65]
	ds_read_b128 v[130:133], v236 offset:34912
	s_waitcnt lgkmcnt(3)
	v_mfma_f32_32x32x16_f16 v[114:129], v[134:137], v[162:165], v[114:129]
	v_mfma_f32_32x32x16_f16 v[34:49], v[134:137], v[166:169], v[34:49]
	ds_read_b128 v[134:137], v236 offset:39264
	s_waitcnt lgkmcnt(3)
	v_mfma_f32_32x32x16_f16 v[98:113], v[138:141], v[162:165], v[98:113]
	v_mfma_f32_32x32x16_f16 v[18:33], v[138:141], v[166:169], v[18:33]
	ds_read_b128 v[138:141], v236 offset:43616
	s_waitcnt lgkmcnt(3)
	v_mfma_f32_32x32x16_f16 v[66:81], v[142:145], v[162:165], v[66:81]
	v_mfma_f32_32x32x16_f16 v[2:17], v[142:145], v[166:169], v[2:17]
	ds_read_b128 v[142:145], v236 offset:47968
	global_load_dwordx4 v[162:165], v239, s[56:57]
	global_load_dwordx4 v[166:169], v239, s[56:57] offset:512
	s_add_u32 s56, s56, 0x4000
	s_addc_u32 s57, s57, 0
	s_waitcnt vmcnt(8)
	s_waitcnt lgkmcnt(3)
	v_mfma_f32_32x32x16_f16 v[82:97], v[130:133], v[170:173], v[82:97]
	v_mfma_f32_32x32x16_f16 v[50:65], v[130:133], v[174:177], v[50:65]
	ds_read_b128 v[130:133], v236 offset:34944
	s_waitcnt lgkmcnt(3)
	v_mfma_f32_32x32x16_f16 v[114:129], v[134:137], v[170:173], v[114:129]
	v_mfma_f32_32x32x16_f16 v[34:49], v[134:137], v[174:177], v[34:49]
	ds_read_b128 v[134:137], v236 offset:39296
	s_waitcnt lgkmcnt(3)
	v_mfma_f32_32x32x16_f16 v[98:113], v[138:141], v[170:173], v[98:113]
	v_mfma_f32_32x32x16_f16 v[18:33], v[138:141], v[174:177], v[18:33]
	ds_read_b128 v[138:141], v236 offset:43648
	s_waitcnt lgkmcnt(3)
	v_mfma_f32_32x32x16_f16 v[66:81], v[142:145], v[170:173], v[66:81]
	v_mfma_f32_32x32x16_f16 v[2:17], v[142:145], v[174:177], v[2:17]
	ds_read_b128 v[142:145], v236 offset:48000
	global_load_dwordx4 v[170:173], v239, s[56:57]
	global_load_dwordx4 v[174:177], v239, s[56:57] offset:512
	s_add_u32 s56, s56, 0x4000
	s_addc_u32 s57, s57, 0
	s_waitcnt vmcnt(8)
	s_waitcnt lgkmcnt(3)
	v_mfma_f32_32x32x16_f16 v[82:97], v[130:133], v[178:181], v[82:97]
	v_mfma_f32_32x32x16_f16 v[50:65], v[130:133], v[182:185], v[50:65]
	ds_read_b128 v[130:133], v236 offset:34976
	s_waitcnt lgkmcnt(3)
	v_mfma_f32_32x32x16_f16 v[114:129], v[134:137], v[178:181], v[114:129]
	v_mfma_f32_32x32x16_f16 v[34:49], v[134:137], v[182:185], v[34:49]
	ds_read_b128 v[134:137], v236 offset:39328
	s_waitcnt lgkmcnt(3)
	v_mfma_f32_32x32x16_f16 v[98:113], v[138:141], v[178:181], v[98:113]
	v_mfma_f32_32x32x16_f16 v[18:33], v[138:141], v[182:185], v[18:33]
	ds_read_b128 v[138:141], v236 offset:43680
	s_waitcnt lgkmcnt(3)
	v_mfma_f32_32x32x16_f16 v[66:81], v[142:145], v[178:181], v[66:81]
	v_mfma_f32_32x32x16_f16 v[2:17], v[142:145], v[182:185], v[2:17]
	ds_read_b128 v[142:145], v236 offset:48032
	global_load_dwordx4 v[178:181], v239, s[56:57]
	global_load_dwordx4 v[182:185], v239, s[56:57] offset:512
	s_add_u32 s56, s56, 0x4000
	s_addc_u32 s57, s57, 0
	s_waitcnt vmcnt(8)
	s_waitcnt lgkmcnt(3)
	v_mfma_f32_32x32x16_f16 v[82:97], v[130:133], v[146:149], v[82:97]
	v_mfma_f32_32x32x16_f16 v[50:65], v[130:133], v[150:153], v[50:65]
	ds_read_b128 v[130:133], v236 offset:35008
	s_waitcnt lgkmcnt(3)
	v_mfma_f32_32x32x16_f16 v[114:129], v[134:137], v[146:149], v[114:129]
	v_mfma_f32_32x32x16_f16 v[34:49], v[134:137], v[150:153], v[34:49]
	ds_read_b128 v[134:137], v236 offset:39360
	s_waitcnt lgkmcnt(3)
	v_mfma_f32_32x32x16_f16 v[98:113], v[138:141], v[146:149], v[98:113]
	v_mfma_f32_32x32x16_f16 v[18:33], v[138:141], v[150:153], v[18:33]
	ds_read_b128 v[138:141], v236 offset:43712
	s_waitcnt lgkmcnt(3)
	v_mfma_f32_32x32x16_f16 v[66:81], v[142:145], v[146:149], v[66:81]
	v_mfma_f32_32x32x16_f16 v[2:17], v[142:145], v[150:153], v[2:17]
	ds_read_b128 v[142:145], v236 offset:48064
	global_load_dwordx4 v[146:149], v239, s[56:57]
	global_load_dwordx4 v[150:153], v239, s[56:57] offset:512
	s_add_u32 s56, s56, 0x4000
	s_addc_u32 s57, s57, 0
	s_waitcnt vmcnt(23)
	v_cvt_pk_f16_f32 v204, v204, v205
	v_cvt_pk_f16_f32 v205, v206, v207
	ds_write_b64 v237, v[204:205]
	s_waitcnt vmcnt(22)
	v_cvt_pk_f16_f32 v208, v208, v209
	v_cvt_pk_f16_f32 v209, v210, v211
	ds_write_b64 v237, v[208:209] offset:4352
	s_waitcnt vmcnt(21)
	v_cvt_pk_f16_f32 v212, v212, v213
	v_cvt_pk_f16_f32 v213, v214, v215
	ds_write_b64 v237, v[212:213] offset:8704
	s_waitcnt vmcnt(20)
	v_cvt_pk_f16_f32 v216, v216, v217
	v_cvt_pk_f16_f32 v217, v218, v219
	ds_write_b64 v237, v[216:217] offset:13056
	s_waitcnt vmcnt(19)
	v_cvt_pk_f16_f32 v220, v220, v221
	v_cvt_pk_f16_f32 v221, v222, v223
	ds_write_b64 v237, v[220:221] offset:17408
	s_waitcnt vmcnt(18)
	v_cvt_pk_f16_f32 v224, v224, v225
	v_cvt_pk_f16_f32 v225, v226, v227
	ds_write_b64 v237, v[224:225] offset:21760
	s_waitcnt vmcnt(17)
	v_cvt_pk_f16_f32 v228, v228, v229
	v_cvt_pk_f16_f32 v229, v230, v231
	ds_write_b64 v237, v[228:229] offset:26112
	s_waitcnt vmcnt(16)
	v_cvt_pk_f16_f32 v232, v232, v233
	v_cvt_pk_f16_f32 v233, v234, v235
	ds_write_b64 v237, v[232:233] offset:30464
	global_load_dwordx4 v[204:207], v238, s[40:41] offset:3584 nt
	global_load_dwordx4 v[208:211], v238, s[42:43] offset:3584 nt
	global_load_dwordx4 v[212:215], v238, s[44:45] offset:3584 nt
	global_load_dwordx4 v[216:219], v238, s[46:47] offset:3584 nt
	global_load_dwordx4 v[220:223], v238, s[48:49] offset:3584 nt
	global_load_dwordx4 v[224:227], v238, s[50:51] offset:3584 nt
	global_load_dwordx4 v[228:231], v238, s[52:53] offset:3584 nt
	global_load_dwordx4 v[232:235], v238, s[54:55] offset:3584 nt
	s_waitcnt vmcnt(16)
	s_waitcnt lgkmcnt(11)
	v_mfma_f32_32x32x16_f16 v[82:97], v[130:133], v[154:157], v[82:97]
	v_mfma_f32_32x32x16_f16 v[50:65], v[130:133], v[158:161], v[50:65]
	ds_read_b128 v[130:133], v236 offset:35040
	s_waitcnt lgkmcnt(11)
	v_mfma_f32_32x32x16_f16 v[114:129], v[134:137], v[154:157], v[114:129]
	v_mfma_f32_32x32x16_f16 v[34:49], v[134:137], v[158:161], v[34:49]
	ds_read_b128 v[134:137], v236 offset:39392
	s_waitcnt lgkmcnt(11)
	v_mfma_f32_32x32x16_f16 v[98:113], v[138:141], v[154:157], v[98:113]
	v_mfma_f32_32x32x16_f16 v[18:33], v[138:141], v[158:161], v[18:33]
	ds_read_b128 v[138:141], v236 offset:43744
	s_waitcnt lgkmcnt(11)
	v_mfma_f32_32x32x16_f16 v[66:81], v[142:145], v[154:157], v[66:81]
	v_mfma_f32_32x32x16_f16 v[2:17], v[142:145], v[158:161], v[2:17]
	ds_read_b128 v[142:145], v236 offset:48096
	global_load_dwordx4 v[154:157], v239, s[56:57]
	global_load_dwordx4 v[158:161], v239, s[56:57] offset:512
	s_add_u32 s56, s56, 0x4000
	s_addc_u32 s57, s57, 0
	s_waitcnt vmcnt(16)
	s_waitcnt lgkmcnt(3)
	v_mfma_f32_32x32x16_f16 v[82:97], v[130:133], v[162:165], v[82:97]
	v_mfma_f32_32x32x16_f16 v[50:65], v[130:133], v[166:169], v[50:65]
	s_waitcnt lgkmcnt(2)
	v_mfma_f32_32x32x16_f16 v[114:129], v[134:137], v[162:165], v[114:129]
	v_mfma_f32_32x32x16_f16 v[34:49], v[134:137], v[166:169], v[34:49]
	s_waitcnt lgkmcnt(1)
	v_mfma_f32_32x32x16_f16 v[98:113], v[138:141], v[162:165], v[98:113]
	v_mfma_f32_32x32x16_f16 v[18:33], v[138:141], v[166:169], v[18:33]
	s_waitcnt lgkmcnt(0)
	v_mfma_f32_32x32x16_f16 v[66:81], v[142:145], v[162:165], v[66:81]
	v_mfma_f32_32x32x16_f16 v[2:17], v[142:145], v[166:169], v[2:17]
	global_load_dwordx4 v[162:165], v239, s[56:57]
	global_load_dwordx4 v[166:169], v239, s[56:57] offset:512
	s_add_u32 s56, s56, 0x4000
	s_addc_u32 s57, s57, 0
	s_waitcnt lgkmcnt(0)
	s_barrier
	ds_read_b128 v[130:133], v236
	ds_read_b128 v[134:137], v236 offset:4352
	ds_read_b128 v[138:141], v236 offset:8704
	ds_read_b128 v[142:145], v236 offset:13056
	s_waitcnt vmcnt(16)
	s_waitcnt lgkmcnt(3)
	v_mfma_f32_32x32x16_f16 v[82:97], v[130:133], v[170:173], v[82:97]
	v_mfma_f32_32x32x16_f16 v[50:65], v[130:133], v[174:177], v[50:65]
	ds_read_b128 v[130:133], v236 offset:32
	s_waitcnt lgkmcnt(3)
	v_mfma_f32_32x32x16_f16 v[114:129], v[134:137], v[170:173], v[114:129]
	v_mfma_f32_32x32x16_f16 v[34:49], v[134:137], v[174:177], v[34:49]
	ds_read_b128 v[134:137], v236 offset:4384
	s_waitcnt lgkmcnt(3)
	v_mfma_f32_32x32x16_f16 v[98:113], v[138:141], v[170:173], v[98:113]
	v_mfma_f32_32x32x16_f16 v[18:33], v[138:141], v[174:177], v[18:33]
	ds_read_b128 v[138:141], v236 offset:8736
	s_waitcnt lgkmcnt(3)
	v_mfma_f32_32x32x16_f16 v[66:81], v[142:145], v[170:173], v[66:81]
	v_mfma_f32_32x32x16_f16 v[2:17], v[142:145], v[174:177], v[2:17]
	ds_read_b128 v[142:145], v236 offset:13088
	global_load_dwordx4 v[170:173], v239, s[56:57]
	global_load_dwordx4 v[174:177], v239, s[56:57] offset:512
	s_add_u32 s56, s56, 0x4000
	s_addc_u32 s57, s57, 0
	s_waitcnt vmcnt(16)
	s_waitcnt lgkmcnt(3)
	v_mfma_f32_32x32x16_f16 v[82:97], v[130:133], v[178:181], v[82:97]
	v_mfma_f32_32x32x16_f16 v[50:65], v[130:133], v[182:185], v[50:65]
	ds_read_b128 v[130:133], v236 offset:64
	s_waitcnt lgkmcnt(3)
	v_mfma_f32_32x32x16_f16 v[114:129], v[134:137], v[178:181], v[114:129]
	v_mfma_f32_32x32x16_f16 v[34:49], v[134:137], v[182:185], v[34:49]
	ds_read_b128 v[134:137], v236 offset:4416
	s_waitcnt lgkmcnt(3)
	v_mfma_f32_32x32x16_f16 v[98:113], v[138:141], v[178:181], v[98:113]
	v_mfma_f32_32x32x16_f16 v[18:33], v[138:141], v[182:185], v[18:33]
	ds_read_b128 v[138:141], v236 offset:8768
	s_waitcnt lgkmcnt(3)
	v_mfma_f32_32x32x16_f16 v[66:81], v[142:145], v[178:181], v[66:81]
	v_mfma_f32_32x32x16_f16 v[2:17], v[142:145], v[182:185], v[2:17]
	ds_read_b128 v[142:145], v236 offset:13120
	global_load_dwordx4 v[178:181], v239, s[56:57]
	global_load_dwordx4 v[182:185], v239, s[56:57] offset:512
	s_add_u32 s56, s56, 0x4000
	s_addc_u32 s57, s57, 0
	s_waitcnt vmcnt(16)
	s_waitcnt lgkmcnt(3)
	v_mfma_f32_32x32x16_f16 v[82:97], v[130:133], v[146:149], v[82:97]
	v_mfma_f32_32x32x16_f16 v[50:65], v[130:133], v[150:153], v[50:65]
	ds_read_b128 v[130:133], v236 offset:96
	s_waitcnt lgkmcnt(3)
	v_mfma_f32_32x32x16_f16 v[114:129], v[134:137], v[146:149], v[114:129]
	v_mfma_f32_32x32x16_f16 v[34:49], v[134:137], v[150:153], v[34:49]
	ds_read_b128 v[134:137], v236 offset:4448
	s_waitcnt lgkmcnt(3)
	v_mfma_f32_32x32x16_f16 v[98:113], v[138:141], v[146:149], v[98:113]
	v_mfma_f32_32x32x16_f16 v[18:33], v[138:141], v[150:153], v[18:33]
	ds_read_b128 v[138:141], v236 offset:8800
	s_waitcnt lgkmcnt(3)
	v_mfma_f32_32x32x16_f16 v[66:81], v[142:145], v[146:149], v[66:81]
	v_mfma_f32_32x32x16_f16 v[2:17], v[142:145], v[150:153], v[2:17]
	ds_read_b128 v[142:145], v236 offset:13152
	global_load_dwordx4 v[146:149], v239, s[56:57]
	global_load_dwordx4 v[150:153], v239, s[56:57] offset:512
	s_add_u32 s56, s56, 0x4000
	s_addc_u32 s57, s57, 0
	s_waitcnt vmcnt(8)
	s_waitcnt lgkmcnt(3)
	v_mfma_f32_32x32x16_f16 v[82:97], v[130:133], v[154:157], v[82:97]
	v_mfma_f32_32x32x16_f16 v[50:65], v[130:133], v[158:161], v[50:65]
	ds_read_b128 v[130:133], v236 offset:128
	s_waitcnt lgkmcnt(3)
	v_mfma_f32_32x32x16_f16 v[114:129], v[134:137], v[154:157], v[114:129]
	v_mfma_f32_32x32x16_f16 v[34:49], v[134:137], v[158:161], v[34:49]
	ds_read_b128 v[134:137], v236 offset:4480
	s_waitcnt lgkmcnt(3)
	v_mfma_f32_32x32x16_f16 v[98:113], v[138:141], v[154:157], v[98:113]
	v_mfma_f32_32x32x16_f16 v[18:33], v[138:141], v[158:161], v[18:33]
	ds_read_b128 v[138:141], v236 offset:8832
	s_waitcnt lgkmcnt(3)
	v_mfma_f32_32x32x16_f16 v[66:81], v[142:145], v[154:157], v[66:81]
	v_mfma_f32_32x32x16_f16 v[2:17], v[142:145], v[158:161], v[2:17]
	ds_read_b128 v[142:145], v236 offset:13184
	global_load_dwordx4 v[154:157], v239, s[56:57]
	global_load_dwordx4 v[158:161], v239, s[56:57] offset:512
	s_add_u32 s56, s56, 0x4000
	s_addc_u32 s57, s57, 0
	s_waitcnt vmcnt(8)
	s_waitcnt lgkmcnt(3)
	v_mfma_f32_32x32x16_f16 v[82:97], v[130:133], v[162:165], v[82:97]
	v_mfma_f32_32x32x16_f16 v[50:65], v[130:133], v[166:169], v[50:65]
	ds_read_b128 v[130:133], v236 offset:160
	s_waitcnt lgkmcnt(3)
	v_mfma_f32_32x32x16_f16 v[114:129], v[134:137], v[162:165], v[114:129]
	v_mfma_f32_32x32x16_f16 v[34:49], v[134:137], v[166:169], v[34:49]
	ds_read_b128 v[134:137], v236 offset:4512
	s_waitcnt lgkmcnt(3)
	v_mfma_f32_32x32x16_f16 v[98:113], v[138:141], v[162:165], v[98:113]
	v_mfma_f32_32x32x16_f16 v[18:33], v[138:141], v[166:169], v[18:33]
	ds_read_b128 v[138:141], v236 offset:8864
	s_waitcnt lgkmcnt(3)
	v_mfma_f32_32x32x16_f16 v[66:81], v[142:145], v[162:165], v[66:81]
	v_mfma_f32_32x32x16_f16 v[2:17], v[142:145], v[166:169], v[2:17]
	ds_read_b128 v[142:145], v236 offset:13216
	global_load_dwordx4 v[162:165], v239, s[56:57]
	global_load_dwordx4 v[166:169], v239, s[56:57] offset:512
	s_add_u32 s56, s56, 0x4000
	s_addc_u32 s57, s57, 0
	s_waitcnt vmcnt(8)
	s_waitcnt lgkmcnt(3)
	v_mfma_f32_32x32x16_f16 v[82:97], v[130:133], v[170:173], v[82:97]
	v_mfma_f32_32x32x16_f16 v[50:65], v[130:133], v[174:177], v[50:65]
	ds_read_b128 v[130:133], v236 offset:192
	s_waitcnt lgkmcnt(3)
	v_mfma_f32_32x32x16_f16 v[114:129], v[134:137], v[170:173], v[114:129]
	v_mfma_f32_32x32x16_f16 v[34:49], v[134:137], v[174:177], v[34:49]
	ds_read_b128 v[134:137], v236 offset:4544
	s_waitcnt lgkmcnt(3)
	v_mfma_f32_32x32x16_f16 v[98:113], v[138:141], v[170:173], v[98:113]
	v_mfma_f32_32x32x16_f16 v[18:33], v[138:141], v[174:177], v[18:33]
	ds_read_b128 v[138:141], v236 offset:8896
	s_waitcnt lgkmcnt(3)
	v_mfma_f32_32x32x16_f16 v[66:81], v[142:145], v[170:173], v[66:81]
	v_mfma_f32_32x32x16_f16 v[2:17], v[142:145], v[174:177], v[2:17]
	ds_read_b128 v[142:145], v236 offset:13248
	global_load_dwordx4 v[170:173], v239, s[56:57]
	global_load_dwordx4 v[174:177], v239, s[56:57] offset:512
	s_add_u32 s56, s56, 0x4000
	s_addc_u32 s57, s57, 0
	s_waitcnt vmcnt(23)
	v_cvt_pk_f16_f32 v204, v204, v205
	v_cvt_pk_f16_f32 v205, v206, v207
	ds_write_b64 v237, v[204:205] offset:34816
	s_waitcnt vmcnt(22)
	v_cvt_pk_f16_f32 v208, v208, v209
	v_cvt_pk_f16_f32 v209, v210, v211
	ds_write_b64 v237, v[208:209] offset:39168
	s_waitcnt vmcnt(21)
	v_cvt_pk_f16_f32 v212, v212, v213
	v_cvt_pk_f16_f32 v213, v214, v215
	ds_write_b64 v237, v[212:213] offset:43520
	s_waitcnt vmcnt(20)
	v_cvt_pk_f16_f32 v216, v216, v217
	v_cvt_pk_f16_f32 v217, v218, v219
	ds_write_b64 v237, v[216:217] offset:47872
	s_waitcnt vmcnt(19)
	v_cvt_pk_f16_f32 v220, v220, v221
	v_cvt_pk_f16_f32 v221, v222, v223
	ds_write_b64 v237, v[220:221] offset:52224
	s_waitcnt vmcnt(18)
	v_cvt_pk_f16_f32 v224, v224, v225
	v_cvt_pk_f16_f32 v225, v226, v227
	ds_write_b64 v237, v[224:225] offset:56576
	s_waitcnt vmcnt(17)
	v_cvt_pk_f16_f32 v228, v228, v229
	v_cvt_pk_f16_f32 v229, v230, v231
	ds_write_b64 v237, v[228:229] offset:60928
	s_waitcnt vmcnt(16)
	v_cvt_pk_f16_f32 v232, v232, v233
	v_cvt_pk_f16_f32 v233, v234, v235
	ds_write_b64 v237, v[232:233] offset:65280
	s_waitcnt vmcnt(8)
	s_waitcnt lgkmcnt(11)
	v_mfma_f32_32x32x16_f16 v[82:97], v[130:133], v[178:181], v[82:97]
	v_mfma_f32_32x32x16_f16 v[50:65], v[130:133], v[182:185], v[50:65]
	ds_read_b128 v[130:133], v236 offset:224
	s_waitcnt lgkmcnt(11)
	v_mfma_f32_32x32x16_f16 v[114:129], v[134:137], v[178:181], v[114:129]
	v_mfma_f32_32x32x16_f16 v[34:49], v[134:137], v[182:185], v[34:49]
	ds_read_b128 v[134:137], v236 offset:4576
	s_waitcnt lgkmcnt(11)
	v_mfma_f32_32x32x16_f16 v[98:113], v[138:141], v[178:181], v[98:113]
	v_mfma_f32_32x32x16_f16 v[18:33], v[138:141], v[182:185], v[18:33]
	ds_read_b128 v[138:141], v236 offset:8928
	s_waitcnt lgkmcnt(11)
	v_mfma_f32_32x32x16_f16 v[66:81], v[142:145], v[178:181], v[66:81]
	v_mfma_f32_32x32x16_f16 v[2:17], v[142:145], v[182:185], v[2:17]
	ds_read_b128 v[142:145], v236 offset:13280
	global_load_dwordx4 v[178:181], v239, s[56:57]
	global_load_dwordx4 v[182:185], v239, s[56:57] offset:512
	s_add_u32 s56, s56, 0x4000
	s_addc_u32 s57, s57, 0
	s_waitcnt vmcnt(8)
	s_waitcnt lgkmcnt(3)
	v_mfma_f32_32x32x16_f16 v[82:97], v[130:133], v[146:149], v[82:97]
	v_mfma_f32_32x32x16_f16 v[50:65], v[130:133], v[150:153], v[50:65]
	s_waitcnt lgkmcnt(2)
	v_mfma_f32_32x32x16_f16 v[114:129], v[134:137], v[146:149], v[114:129]
	v_mfma_f32_32x32x16_f16 v[34:49], v[134:137], v[150:153], v[34:49]
	s_waitcnt lgkmcnt(1)
	v_mfma_f32_32x32x16_f16 v[98:113], v[138:141], v[146:149], v[98:113]
	v_mfma_f32_32x32x16_f16 v[18:33], v[138:141], v[150:153], v[18:33]
	s_waitcnt lgkmcnt(0)
	v_mfma_f32_32x32x16_f16 v[66:81], v[142:145], v[146:149], v[66:81]
	v_mfma_f32_32x32x16_f16 v[2:17], v[142:145], v[150:153], v[2:17]
	global_load_dwordx4 v[146:149], v239, s[56:57]
	global_load_dwordx4 v[150:153], v239, s[56:57] offset:512
	s_add_u32 s56, s56, 0x4000
	s_addc_u32 s57, s57, 0
	s_waitcnt lgkmcnt(0)
	s_barrier
	ds_read_b128 v[130:133], v236 offset:34816
	ds_read_b128 v[134:137], v236 offset:39168
	ds_read_b128 v[138:141], v236 offset:43520
	ds_read_b128 v[142:145], v236 offset:47872
	s_waitcnt vmcnt(8)
	s_waitcnt lgkmcnt(3)
	v_mfma_f32_32x32x16_f16 v[82:97], v[130:133], v[154:157], v[82:97]
	v_mfma_f32_32x32x16_f16 v[50:65], v[130:133], v[158:161], v[50:65]
	ds_read_b128 v[130:133], v236 offset:34848
	s_waitcnt lgkmcnt(3)
	v_mfma_f32_32x32x16_f16 v[114:129], v[134:137], v[154:157], v[114:129]
	v_mfma_f32_32x32x16_f16 v[34:49], v[134:137], v[158:161], v[34:49]
	ds_read_b128 v[134:137], v236 offset:39200
	s_waitcnt lgkmcnt(3)
	v_mfma_f32_32x32x16_f16 v[98:113], v[138:141], v[154:157], v[98:113]
	v_mfma_f32_32x32x16_f16 v[18:33], v[138:141], v[158:161], v[18:33]
	ds_read_b128 v[138:141], v236 offset:43552
	s_waitcnt lgkmcnt(3)
	v_mfma_f32_32x32x16_f16 v[66:81], v[142:145], v[154:157], v[66:81]
	v_mfma_f32_32x32x16_f16 v[2:17], v[142:145], v[158:161], v[2:17]
	ds_read_b128 v[142:145], v236 offset:47904
	global_load_dwordx4 v[154:157], v239, s[56:57]
	global_load_dwordx4 v[158:161], v239, s[56:57] offset:512
	s_add_u32 s56, s56, 0x4000
	s_addc_u32 s57, s57, 0
	s_waitcnt vmcnt(8)
	s_waitcnt lgkmcnt(3)
	v_mfma_f32_32x32x16_f16 v[82:97], v[130:133], v[162:165], v[82:97]
	v_mfma_f32_32x32x16_f16 v[50:65], v[130:133], v[166:169], v[50:65]
	ds_read_b128 v[130:133], v236 offset:34880
	s_waitcnt lgkmcnt(3)
	v_mfma_f32_32x32x16_f16 v[114:129], v[134:137], v[162:165], v[114:129]
	v_mfma_f32_32x32x16_f16 v[34:49], v[134:137], v[166:169], v[34:49]
	ds_read_b128 v[134:137], v236 offset:39232
	s_waitcnt lgkmcnt(3)
	v_mfma_f32_32x32x16_f16 v[98:113], v[138:141], v[162:165], v[98:113]
	v_mfma_f32_32x32x16_f16 v[18:33], v[138:141], v[166:169], v[18:33]
	ds_read_b128 v[138:141], v236 offset:43584
	s_waitcnt lgkmcnt(3)
	v_mfma_f32_32x32x16_f16 v[66:81], v[142:145], v[162:165], v[66:81]
	v_mfma_f32_32x32x16_f16 v[2:17], v[142:145], v[166:169], v[2:17]
	ds_read_b128 v[142:145], v236 offset:47936
	global_load_dwordx4 v[162:165], v239, s[56:57]
	global_load_dwordx4 v[166:169], v239, s[56:57] offset:512
	s_add_u32 s56, s56, 0x4000
	s_addc_u32 s57, s57, 0
	s_waitcnt vmcnt(8)
	s_waitcnt lgkmcnt(3)
	v_mfma_f32_32x32x16_f16 v[82:97], v[130:133], v[170:173], v[82:97]
	v_mfma_f32_32x32x16_f16 v[50:65], v[130:133], v[174:177], v[50:65]
	ds_read_b128 v[130:133], v236 offset:34912
	s_waitcnt lgkmcnt(3)
	v_mfma_f32_32x32x16_f16 v[114:129], v[134:137], v[170:173], v[114:129]
	v_mfma_f32_32x32x16_f16 v[34:49], v[134:137], v[174:177], v[34:49]
	ds_read_b128 v[134:137], v236 offset:39264
	s_waitcnt lgkmcnt(3)
	v_mfma_f32_32x32x16_f16 v[98:113], v[138:141], v[170:173], v[98:113]
	v_mfma_f32_32x32x16_f16 v[18:33], v[138:141], v[174:177], v[18:33]
	ds_read_b128 v[138:141], v236 offset:43616
	s_waitcnt lgkmcnt(3)
	v_mfma_f32_32x32x16_f16 v[66:81], v[142:145], v[170:173], v[66:81]
	v_mfma_f32_32x32x16_f16 v[2:17], v[142:145], v[174:177], v[2:17]
	ds_read_b128 v[142:145], v236 offset:47968
	global_load_dwordx4 v[170:173], v239, s[56:57]
	global_load_dwordx4 v[174:177], v239, s[56:57] offset:512
	s_add_u32 s56, s56, 0x4000
	s_addc_u32 s57, s57, 0
	s_waitcnt vmcnt(8)
	s_waitcnt lgkmcnt(3)
	v_mfma_f32_32x32x16_f16 v[82:97], v[130:133], v[178:181], v[82:97]
	v_mfma_f32_32x32x16_f16 v[50:65], v[130:133], v[182:185], v[50:65]
	ds_read_b128 v[130:133], v236 offset:34944
	s_waitcnt lgkmcnt(3)
	v_mfma_f32_32x32x16_f16 v[114:129], v[134:137], v[178:181], v[114:129]
	v_mfma_f32_32x32x16_f16 v[34:49], v[134:137], v[182:185], v[34:49]
	ds_read_b128 v[134:137], v236 offset:39296
	s_waitcnt lgkmcnt(3)
	v_mfma_f32_32x32x16_f16 v[98:113], v[138:141], v[178:181], v[98:113]
	v_mfma_f32_32x32x16_f16 v[18:33], v[138:141], v[182:185], v[18:33]
	ds_read_b128 v[138:141], v236 offset:43648
	s_waitcnt lgkmcnt(3)
	v_mfma_f32_32x32x16_f16 v[66:81], v[142:145], v[178:181], v[66:81]
	v_mfma_f32_32x32x16_f16 v[2:17], v[142:145], v[182:185], v[2:17]
	ds_read_b128 v[142:145], v236 offset:48000
	s_waitcnt vmcnt(6)
	s_waitcnt lgkmcnt(3)
	v_mfma_f32_32x32x16_f16 v[82:97], v[130:133], v[146:149], v[82:97]
	v_mfma_f32_32x32x16_f16 v[50:65], v[130:133], v[150:153], v[50:65]
	ds_read_b128 v[130:133], v236 offset:34976
	s_waitcnt lgkmcnt(3)
	v_mfma_f32_32x32x16_f16 v[114:129], v[134:137], v[146:149], v[114:129]
	v_mfma_f32_32x32x16_f16 v[34:49], v[134:137], v[150:153], v[34:49]
	ds_read_b128 v[134:137], v236 offset:39328
	s_waitcnt lgkmcnt(3)
	v_mfma_f32_32x32x16_f16 v[98:113], v[138:141], v[146:149], v[98:113]
	v_mfma_f32_32x32x16_f16 v[18:33], v[138:141], v[150:153], v[18:33]
	ds_read_b128 v[138:141], v236 offset:43680
	s_waitcnt lgkmcnt(3)
	v_mfma_f32_32x32x16_f16 v[66:81], v[142:145], v[146:149], v[66:81]
	v_mfma_f32_32x32x16_f16 v[2:17], v[142:145], v[150:153], v[2:17]
	ds_read_b128 v[142:145], v236 offset:48032
	s_waitcnt vmcnt(4)
	s_waitcnt lgkmcnt(3)
	v_mfma_f32_32x32x16_f16 v[82:97], v[130:133], v[154:157], v[82:97]
	v_mfma_f32_32x32x16_f16 v[50:65], v[130:133], v[158:161], v[50:65]
	ds_read_b128 v[130:133], v236 offset:35008
	s_waitcnt lgkmcnt(3)
	v_mfma_f32_32x32x16_f16 v[114:129], v[134:137], v[154:157], v[114:129]
	v_mfma_f32_32x32x16_f16 v[34:49], v[134:137], v[158:161], v[34:49]
	ds_read_b128 v[134:137], v236 offset:39360
	s_waitcnt lgkmcnt(3)
	v_mfma_f32_32x32x16_f16 v[98:113], v[138:141], v[154:157], v[98:113]
	v_mfma_f32_32x32x16_f16 v[18:33], v[138:141], v[158:161], v[18:33]
	ds_read_b128 v[138:141], v236 offset:43712
	s_waitcnt lgkmcnt(3)
	v_mfma_f32_32x32x16_f16 v[66:81], v[142:145], v[154:157], v[66:81]
	v_mfma_f32_32x32x16_f16 v[2:17], v[142:145], v[158:161], v[2:17]
	ds_read_b128 v[142:145], v236 offset:48064
	s_waitcnt vmcnt(2)
	s_waitcnt lgkmcnt(3)
	v_mfma_f32_32x32x16_f16 v[82:97], v[130:133], v[162:165], v[82:97]
	v_mfma_f32_32x32x16_f16 v[50:65], v[130:133], v[166:169], v[50:65]
	ds_read_b128 v[130:133], v236 offset:35040
	s_waitcnt lgkmcnt(3)
	v_mfma_f32_32x32x16_f16 v[114:129], v[134:137], v[162:165], v[114:129]
	v_mfma_f32_32x32x16_f16 v[34:49], v[134:137], v[166:169], v[34:49]
	ds_read_b128 v[134:137], v236 offset:39392
	s_waitcnt lgkmcnt(3)
	v_mfma_f32_32x32x16_f16 v[98:113], v[138:141], v[162:165], v[98:113]
	v_mfma_f32_32x32x16_f16 v[18:33], v[138:141], v[166:169], v[18:33]
	ds_read_b128 v[138:141], v236 offset:43744
	s_waitcnt lgkmcnt(3)
	v_mfma_f32_32x32x16_f16 v[66:81], v[142:145], v[162:165], v[66:81]
	v_mfma_f32_32x32x16_f16 v[2:17], v[142:145], v[166:169], v[2:17]
	ds_read_b128 v[142:145], v236 offset:48096
	s_waitcnt vmcnt(0)
	s_waitcnt lgkmcnt(3)
	v_mfma_f32_32x32x16_f16 v[82:97], v[130:133], v[170:173], v[82:97]
	v_mfma_f32_32x32x16_f16 v[50:65], v[130:133], v[174:177], v[50:65]
	s_waitcnt lgkmcnt(2)
	v_mfma_f32_32x32x16_f16 v[114:129], v[134:137], v[170:173], v[114:129]
	v_mfma_f32_32x32x16_f16 v[34:49], v[134:137], v[174:177], v[34:49]
	s_waitcnt lgkmcnt(1)
	v_mfma_f32_32x32x16_f16 v[98:113], v[138:141], v[170:173], v[98:113]
	v_mfma_f32_32x32x16_f16 v[18:33], v[138:141], v[174:177], v[18:33]
	s_waitcnt lgkmcnt(0)
	v_mfma_f32_32x32x16_f16 v[66:81], v[142:145], v[170:173], v[66:81]
	v_mfma_f32_32x32x16_f16 v[2:17], v[142:145], v[174:177], v[2:17]
	s_waitcnt vmcnt(0) lgkmcnt(0)
	s_nop 15
	s_mov_b64 exec, -1
	v_bfe_u32 v202, v0, 5, 1
	s_lshl_b32 s34, s29, 9
	v_and_b32_e32 v203, 0x1c0, v0
	v_and_b32_e32 v204, 31, v0
	v_or3_b32 v0, s34, v203, v204
	v_lshlrev_b32_e32 v0, 2, v0
	s_waitcnt vmcnt(0) lgkmcnt(0)
	s_barrier
	v_mov_b32_e32 v131, v244
	v_mov_b32_e32 v1, v245
	v_fmamk_f32 v130, v131, 0x80000000, v82
	s_mov_b32 s6, 0x3dcccccd
	s_mov_b32 s7, 0xbdcccccd
	v_fma_f32 v132, v130, s6, 0
	v_fma_f32 v133, v132, s6, 0
	v_fma_f32 v130, -v133, v131, v83
	v_fmac_f32_e32 v132, 0x3dcccccd, v130
	v_fmac_f32_e32 v133, 0x3dcccccd, v132
	v_fma_f32 v130, -v133, v131, v84
	v_fmac_f32_e32 v132, 0x3dcccccd, v130
	v_fmac_f32_e32 v133, 0x3dcccccd, v132
	v_fma_f32 v130, -v133, v131, v85
	v_fmac_f32_e32 v132, 0x3dcccccd, v130
	v_fmac_f32_e32 v133, 0x3dcccccd, v132
	v_fma_f32 v130, -v133, v131, v86
	v_fmac_f32_e32 v132, 0x3dcccccd, v130
	v_fmac_f32_e32 v133, 0x3dcccccd, v132
	v_fma_f32 v130, -v133, v131, v87
	v_fmac_f32_e32 v132, 0x3dcccccd, v130
	v_fmac_f32_e32 v133, 0x3dcccccd, v132
	v_fma_f32 v130, -v133, v131, v88
	v_fmac_f32_e32 v132, 0x3dcccccd, v130
	v_fmac_f32_e32 v133, 0x3dcccccd, v132
	v_fma_f32 v130, -v133, v131, v89
	v_fmac_f32_e32 v132, 0x3dcccccd, v130
	v_fmac_f32_e32 v133, 0x3dcccccd, v132
	v_fma_f32 v130, -v133, v131, v90
	v_fmac_f32_e32 v132, 0x3dcccccd, v130
	v_fmac_f32_e32 v133, 0x3dcccccd, v132
	v_fma_f32 v130, -v133, v131, v91
	v_fmac_f32_e32 v132, 0x3dcccccd, v130
	v_fmac_f32_e32 v133, 0x3dcccccd, v132
	v_fma_f32 v130, -v133, v131, v92
	v_fmac_f32_e32 v132, 0x3dcccccd, v130
	v_fmac_f32_e32 v133, 0x3dcccccd, v132
	v_fma_f32 v130, -v133, v131, v93
	v_fmac_f32_e32 v132, 0x3dcccccd, v130
	v_fmac_f32_e32 v133, 0x3dcccccd, v132
	v_fma_f32 v130, -v133, v131, v94
	v_fmac_f32_e32 v132, 0x3dcccccd, v130
	v_fmac_f32_e32 v133, 0x3dcccccd, v132
	v_fma_f32 v130, -v133, v131, v95
	v_fmac_f32_e32 v132, 0x3dcccccd, v130
	v_fmac_f32_e32 v133, 0x3dcccccd, v132
	v_fma_f32 v130, -v133, v131, v96
	v_fmac_f32_e32 v132, 0x3dcccccd, v130
	v_fmac_f32_e32 v133, 0x3dcccccd, v132
	v_fma_f32 v130, -v133, v131, v97
	v_fmac_f32_e32 v132, 0x3dcccccd, v130
	v_fmac_f32_e32 v133, 0x3dcccccd, v132
	v_fma_f32 v130, -v133, v131, v114
	v_fmac_f32_e32 v132, 0x3dcccccd, v130
	v_fmac_f32_e32 v133, 0x3dcccccd, v132
	v_fma_f32 v130, -v133, v131, v115
	v_fmac_f32_e32 v132, 0x3dcccccd, v130
	v_fmac_f32_e32 v133, 0x3dcccccd, v132
	v_fma_f32 v130, -v133, v131, v116
	v_fmac_f32_e32 v132, 0x3dcccccd, v130
	v_fmac_f32_e32 v133, 0x3dcccccd, v132
	v_fma_f32 v130, -v133, v131, v117
	v_fmac_f32_e32 v132, 0x3dcccccd, v130
	v_fmac_f32_e32 v133, 0x3dcccccd, v132
	v_fma_f32 v130, -v133, v131, v118
	v_fmac_f32_e32 v132, 0x3dcccccd, v130
	v_fmac_f32_e32 v133, 0x3dcccccd, v132
	v_fma_f32 v130, -v133, v131, v119
	v_fmac_f32_e32 v132, 0x3dcccccd, v130
	v_fmac_f32_e32 v133, 0x3dcccccd, v132
	v_fma_f32 v130, -v133, v131, v120
	v_fmac_f32_e32 v132, 0x3dcccccd, v130
	v_fmac_f32_e32 v133, 0x3dcccccd, v132
	v_fma_f32 v130, -v133, v131, v121
	v_fmac_f32_e32 v132, 0x3dcccccd, v130
	v_fmac_f32_e32 v133, 0x3dcccccd, v132
	v_fma_f32 v130, -v133, v131, v122
	v_fmac_f32_e32 v132, 0x3dcccccd, v130
	v_fmac_f32_e32 v133, 0x3dcccccd, v132
	v_fma_f32 v130, -v133, v131, v123
	v_fmac_f32_e32 v132, 0x3dcccccd, v130
	v_fmac_f32_e32 v133, 0x3dcccccd, v132
	v_fma_f32 v130, -v133, v131, v124
	v_fmac_f32_e32 v132, 0x3dcccccd, v130
	v_fmac_f32_e32 v133, 0x3dcccccd, v132
	v_fma_f32 v130, -v133, v131, v125
	v_fmac_f32_e32 v132, 0x3dcccccd, v130
	v_fmac_f32_e32 v133, 0x3dcccccd, v132
	v_fma_f32 v130, -v133, v131, v126
	v_fmac_f32_e32 v132, 0x3dcccccd, v130
	v_fmac_f32_e32 v133, 0x3dcccccd, v132
	v_fma_f32 v130, -v133, v131, v127
	v_fmac_f32_e32 v132, 0x3dcccccd, v130
	v_fmac_f32_e32 v133, 0x3dcccccd, v132
	v_fma_f32 v130, -v133, v131, v128
	v_fmac_f32_e32 v132, 0x3dcccccd, v130
	v_fmac_f32_e32 v133, 0x3dcccccd, v132
	v_fma_f32 v130, -v133, v131, v129
	v_fmac_f32_e32 v132, 0x3dcccccd, v130
	v_fmac_f32_e32 v133, 0x3dcccccd, v132
	v_fma_f32 v130, -v133, v131, v98
	v_fmac_f32_e32 v132, 0x3dcccccd, v130
	v_fmac_f32_e32 v133, 0x3dcccccd, v132
	v_fma_f32 v130, -v133, v131, v99
	v_fmac_f32_e32 v132, 0x3dcccccd, v130
	v_fmac_f32_e32 v133, 0x3dcccccd, v132
	v_fma_f32 v130, -v133, v131, v100
	v_fmac_f32_e32 v132, 0x3dcccccd, v130
	v_fmac_f32_e32 v133, 0x3dcccccd, v132
	v_fma_f32 v130, -v133, v131, v101
	v_fmac_f32_e32 v132, 0x3dcccccd, v130
	v_fmac_f32_e32 v133, 0x3dcccccd, v132
	v_fma_f32 v130, -v133, v131, v102
	v_fmac_f32_e32 v132, 0x3dcccccd, v130
	v_fmac_f32_e32 v133, 0x3dcccccd, v132
	v_fma_f32 v130, -v133, v131, v103
	v_fmac_f32_e32 v132, 0x3dcccccd, v130
	v_fmac_f32_e32 v133, 0x3dcccccd, v132
	v_fma_f32 v130, -v133, v131, v104
	v_fmac_f32_e32 v132, 0x3dcccccd, v130
	v_fmac_f32_e32 v133, 0x3dcccccd, v132
	v_fma_f32 v130, -v133, v131, v105
	v_fmac_f32_e32 v132, 0x3dcccccd, v130
	v_fmac_f32_e32 v133, 0x3dcccccd, v132
	v_fma_f32 v130, -v133, v131, v106
	v_fmac_f32_e32 v132, 0x3dcccccd, v130
	v_fmac_f32_e32 v133, 0x3dcccccd, v132
	v_fma_f32 v130, -v133, v131, v107
	v_fmac_f32_e32 v132, 0x3dcccccd, v130
	v_fmac_f32_e32 v133, 0x3dcccccd, v132
	v_fma_f32 v130, -v133, v131, v108
	v_fmac_f32_e32 v132, 0x3dcccccd, v130
	v_fmac_f32_e32 v133, 0x3dcccccd, v132
	v_fma_f32 v130, -v133, v131, v109
	v_fmac_f32_e32 v132, 0x3dcccccd, v130
	v_fmac_f32_e32 v133, 0x3dcccccd, v132
	v_fma_f32 v130, -v133, v131, v110
	v_fmac_f32_e32 v132, 0x3dcccccd, v130
	v_fmac_f32_e32 v133, 0x3dcccccd, v132
	v_fma_f32 v130, -v133, v131, v111
	v_fmac_f32_e32 v132, 0x3dcccccd, v130
	v_fmac_f32_e32 v133, 0x3dcccccd, v132
	v_fma_f32 v130, -v133, v131, v112
	v_fmac_f32_e32 v132, 0x3dcccccd, v130
	v_fmac_f32_e32 v133, 0x3dcccccd, v132
	v_fma_f32 v130, -v133, v131, v113
	v_fmac_f32_e32 v132, 0x3dcccccd, v130
	v_fmac_f32_e32 v133, 0x3dcccccd, v132
	v_fma_f32 v130, -v133, v131, v66
	v_fmac_f32_e32 v132, 0x3dcccccd, v130
	v_fmac_f32_e32 v133, 0x3dcccccd, v132
	v_fma_f32 v130, -v133, v131, v67
	v_fmac_f32_e32 v132, 0x3dcccccd, v130
	v_fmac_f32_e32 v133, 0x3dcccccd, v132
	v_fma_f32 v130, -v133, v131, v68
	v_fmac_f32_e32 v132, 0x3dcccccd, v130
	v_fmac_f32_e32 v133, 0x3dcccccd, v132
	v_fma_f32 v130, -v133, v131, v69
	v_fmac_f32_e32 v132, 0x3dcccccd, v130
	v_fmac_f32_e32 v133, 0x3dcccccd, v132
	v_fma_f32 v130, -v133, v131, v70
	v_fmac_f32_e32 v132, 0x3dcccccd, v130
	v_fmac_f32_e32 v133, 0x3dcccccd, v132
	v_fma_f32 v130, -v133, v131, v71
	v_fmac_f32_e32 v132, 0x3dcccccd, v130
	v_fmac_f32_e32 v133, 0x3dcccccd, v132
	v_fma_f32 v130, -v133, v131, v72
	v_fmac_f32_e32 v132, 0x3dcccccd, v130
	v_fmac_f32_e32 v133, 0x3dcccccd, v132
	v_fma_f32 v130, -v133, v131, v73
	v_fmac_f32_e32 v132, 0x3dcccccd, v130
	v_fmac_f32_e32 v133, 0x3dcccccd, v132
	v_fma_f32 v130, -v133, v131, v74
	v_fmac_f32_e32 v132, 0x3dcccccd, v130
	v_fmac_f32_e32 v133, 0x3dcccccd, v132
	v_fma_f32 v130, -v133, v131, v75
	v_fmac_f32_e32 v132, 0x3dcccccd, v130
	v_fmac_f32_e32 v133, 0x3dcccccd, v132
	v_fma_f32 v130, -v133, v131, v76
	v_fmac_f32_e32 v132, 0x3dcccccd, v130
	v_fmac_f32_e32 v133, 0x3dcccccd, v132
	v_fma_f32 v130, -v133, v131, v77
	v_fmac_f32_e32 v132, 0x3dcccccd, v130
	v_fmac_f32_e32 v133, 0x3dcccccd, v132
	v_fma_f32 v130, -v133, v131, v78
	v_fmac_f32_e32 v132, 0x3dcccccd, v130
	v_fmac_f32_e32 v133, 0x3dcccccd, v132
	v_fma_f32 v130, -v133, v131, v79
	v_fmac_f32_e32 v132, 0x3dcccccd, v130
	v_fmac_f32_e32 v133, 0x3dcccccd, v132
	v_fma_f32 v130, -v133, v131, v80
	v_fmac_f32_e32 v132, 0x3dcccccd, v130
	v_fmac_f32_e32 v133, 0x3dcccccd, v132
	v_fma_f32 v130, -v133, v131, v81
	v_fmac_f32_e32 v132, 0x3dcccccd, v130
	v_fmamk_f32 v130, v1, 0x80000000, v50
	v_fma_f32 v134, v130, s6, 0
	v_fma_f32 v135, v134, s6, 0
	v_fma_f32 v130, -v135, v1, v51
	v_fmac_f32_e32 v134, 0x3dcccccd, v130
	v_fmac_f32_e32 v135, 0x3dcccccd, v134
	v_fma_f32 v130, -v135, v1, v52
	v_fmac_f32_e32 v134, 0x3dcccccd, v130
	v_fmac_f32_e32 v135, 0x3dcccccd, v134
	v_fma_f32 v130, -v135, v1, v53
	v_fmac_f32_e32 v134, 0x3dcccccd, v130
	v_fmac_f32_e32 v135, 0x3dcccccd, v134
	v_fma_f32 v130, -v135, v1, v54
	v_fmac_f32_e32 v134, 0x3dcccccd, v130
	v_fmac_f32_e32 v135, 0x3dcccccd, v134
	v_fma_f32 v130, -v135, v1, v55
	v_fmac_f32_e32 v134, 0x3dcccccd, v130
	v_fmac_f32_e32 v135, 0x3dcccccd, v134
	v_fma_f32 v130, -v135, v1, v56
	v_fmac_f32_e32 v134, 0x3dcccccd, v130
	v_fmac_f32_e32 v135, 0x3dcccccd, v134
	v_fma_f32 v130, -v135, v1, v57
	v_fmac_f32_e32 v134, 0x3dcccccd, v130
	v_fmac_f32_e32 v135, 0x3dcccccd, v134
	v_fma_f32 v130, -v135, v1, v58
	v_fmac_f32_e32 v134, 0x3dcccccd, v130
	v_fmac_f32_e32 v135, 0x3dcccccd, v134
	v_fma_f32 v130, -v135, v1, v59
	v_fmac_f32_e32 v134, 0x3dcccccd, v130
	v_fmac_f32_e32 v135, 0x3dcccccd, v134
	v_fma_f32 v130, -v135, v1, v60
	v_fmac_f32_e32 v134, 0x3dcccccd, v130
	v_fmac_f32_e32 v135, 0x3dcccccd, v134
	v_fma_f32 v130, -v135, v1, v61
	v_fmac_f32_e32 v134, 0x3dcccccd, v130
	v_fmac_f32_e32 v135, 0x3dcccccd, v134
	v_fma_f32 v130, -v135, v1, v62
	v_fmac_f32_e32 v134, 0x3dcccccd, v130
	v_fmac_f32_e32 v135, 0x3dcccccd, v134
	v_fma_f32 v130, -v135, v1, v63
	v_fmac_f32_e32 v134, 0x3dcccccd, v130
	v_fmac_f32_e32 v135, 0x3dcccccd, v134
	v_fma_f32 v130, -v135, v1, v64
	v_fmac_f32_e32 v134, 0x3dcccccd, v130
	v_fmac_f32_e32 v135, 0x3dcccccd, v134
	v_fma_f32 v130, -v135, v1, v65
	v_fmac_f32_e32 v134, 0x3dcccccd, v130
	v_fmac_f32_e32 v135, 0x3dcccccd, v134
	v_fma_f32 v130, -v135, v1, v34
	v_fmac_f32_e32 v134, 0x3dcccccd, v130
	v_fmac_f32_e32 v135, 0x3dcccccd, v134
	v_fma_f32 v130, -v135, v1, v35
	v_fmac_f32_e32 v134, 0x3dcccccd, v130
	v_fmac_f32_e32 v135, 0x3dcccccd, v134
	v_fma_f32 v130, -v135, v1, v36
	v_fmac_f32_e32 v134, 0x3dcccccd, v130
	v_fmac_f32_e32 v135, 0x3dcccccd, v134
	v_fma_f32 v130, -v135, v1, v37
	v_fmac_f32_e32 v134, 0x3dcccccd, v130
	v_fmac_f32_e32 v135, 0x3dcccccd, v134
	v_fma_f32 v130, -v135, v1, v38
	v_fmac_f32_e32 v134, 0x3dcccccd, v130
	v_fmac_f32_e32 v135, 0x3dcccccd, v134
	v_fma_f32 v130, -v135, v1, v39
	v_fmac_f32_e32 v134, 0x3dcccccd, v130
	v_fmac_f32_e32 v135, 0x3dcccccd, v134
	v_fma_f32 v130, -v135, v1, v40
	v_fmac_f32_e32 v134, 0x3dcccccd, v130
	v_fmac_f32_e32 v135, 0x3dcccccd, v134
	v_fma_f32 v130, -v135, v1, v41
	v_fmac_f32_e32 v134, 0x3dcccccd, v130
	v_fmac_f32_e32 v135, 0x3dcccccd, v134
	v_fma_f32 v130, -v135, v1, v42
	v_fmac_f32_e32 v134, 0x3dcccccd, v130
	v_fmac_f32_e32 v135, 0x3dcccccd, v134
	v_fma_f32 v130, -v135, v1, v43
	v_fmac_f32_e32 v134, 0x3dcccccd, v130
	v_fmac_f32_e32 v135, 0x3dcccccd, v134
	v_fma_f32 v130, -v135, v1, v44
	v_fmac_f32_e32 v134, 0x3dcccccd, v130
	v_fmac_f32_e32 v135, 0x3dcccccd, v134
	v_fma_f32 v130, -v135, v1, v45
	v_fmac_f32_e32 v134, 0x3dcccccd, v130
	v_fmac_f32_e32 v135, 0x3dcccccd, v134
	v_fma_f32 v130, -v135, v1, v46
	v_fmac_f32_e32 v134, 0x3dcccccd, v130
	v_fmac_f32_e32 v135, 0x3dcccccd, v134
	v_fma_f32 v130, -v135, v1, v47
	v_fmac_f32_e32 v134, 0x3dcccccd, v130
	v_fmac_f32_e32 v135, 0x3dcccccd, v134
	v_fma_f32 v130, -v135, v1, v48
	v_fmac_f32_e32 v134, 0x3dcccccd, v130
	v_fmac_f32_e32 v135, 0x3dcccccd, v134
	v_fma_f32 v130, -v135, v1, v49
	v_fmac_f32_e32 v134, 0x3dcccccd, v130
	v_fmac_f32_e32 v135, 0x3dcccccd, v134
	v_fma_f32 v130, -v135, v1, v18
	v_fmac_f32_e32 v134, 0x3dcccccd, v130
	v_fmac_f32_e32 v135, 0x3dcccccd, v134
	v_fma_f32 v130, -v135, v1, v19
	v_fmac_f32_e32 v134, 0x3dcccccd, v130
	v_fmac_f32_e32 v135, 0x3dcccccd, v134
	v_fma_f32 v130, -v135, v1, v20
	v_fmac_f32_e32 v134, 0x3dcccccd, v130
	v_fmac_f32_e32 v135, 0x3dcccccd, v134
	v_fma_f32 v130, -v135, v1, v21
	v_fmac_f32_e32 v134, 0x3dcccccd, v130
	v_fmac_f32_e32 v135, 0x3dcccccd, v134
	v_fma_f32 v130, -v135, v1, v22
	v_fmac_f32_e32 v134, 0x3dcccccd, v130
	v_fmac_f32_e32 v135, 0x3dcccccd, v134
	v_fma_f32 v130, -v135, v1, v23
	v_fmac_f32_e32 v134, 0x3dcccccd, v130
	v_fmac_f32_e32 v135, 0x3dcccccd, v134
	v_fma_f32 v130, -v135, v1, v24
	v_fmac_f32_e32 v134, 0x3dcccccd, v130
	v_fmac_f32_e32 v135, 0x3dcccccd, v134
	v_fma_f32 v130, -v135, v1, v25
	v_fmac_f32_e32 v134, 0x3dcccccd, v130
	v_fmac_f32_e32 v135, 0x3dcccccd, v134
	v_fma_f32 v130, -v135, v1, v26
	v_fmac_f32_e32 v134, 0x3dcccccd, v130
	v_fmac_f32_e32 v135, 0x3dcccccd, v134
	v_fma_f32 v130, -v135, v1, v27
	v_fmac_f32_e32 v134, 0x3dcccccd, v130
	v_fmac_f32_e32 v135, 0x3dcccccd, v134
	v_fma_f32 v130, -v135, v1, v28
	v_fmac_f32_e32 v134, 0x3dcccccd, v130
	v_fmac_f32_e32 v135, 0x3dcccccd, v134
	v_fma_f32 v130, -v135, v1, v29
	v_fmac_f32_e32 v134, 0x3dcccccd, v130
	v_fmac_f32_e32 v135, 0x3dcccccd, v134
	v_fma_f32 v130, -v135, v1, v30
	v_fmac_f32_e32 v134, 0x3dcccccd, v130
	v_fmac_f32_e32 v135, 0x3dcccccd, v134
	v_fma_f32 v130, -v135, v1, v31
	v_fmac_f32_e32 v134, 0x3dcccccd, v130
	v_fmac_f32_e32 v135, 0x3dcccccd, v134
	v_fma_f32 v130, -v135, v1, v32
	v_fmac_f32_e32 v134, 0x3dcccccd, v130
	v_fmac_f32_e32 v135, 0x3dcccccd, v134
	v_fma_f32 v130, -v135, v1, v33
	v_fmac_f32_e32 v134, 0x3dcccccd, v130
	v_fmac_f32_e32 v135, 0x3dcccccd, v134
	v_fma_f32 v130, -v135, v1, v2
	v_fmac_f32_e32 v134, 0x3dcccccd, v130
	v_fmac_f32_e32 v135, 0x3dcccccd, v134
	v_fma_f32 v130, -v135, v1, v3
	v_fmac_f32_e32 v134, 0x3dcccccd, v130
	v_fmac_f32_e32 v135, 0x3dcccccd, v134
	v_fma_f32 v130, -v135, v1, v4
	v_fmac_f32_e32 v134, 0x3dcccccd, v130
	v_fmac_f32_e32 v135, 0x3dcccccd, v134
	v_fma_f32 v130, -v135, v1, v5
	v_fmac_f32_e32 v134, 0x3dcccccd, v130
	v_fmac_f32_e32 v135, 0x3dcccccd, v134
	v_fma_f32 v130, -v135, v1, v6
	v_fmac_f32_e32 v134, 0x3dcccccd, v130
	v_fmac_f32_e32 v135, 0x3dcccccd, v134
	v_fma_f32 v130, -v135, v1, v7
	v_fmac_f32_e32 v134, 0x3dcccccd, v130
	v_fmac_f32_e32 v135, 0x3dcccccd, v134
	v_fma_f32 v130, -v135, v1, v8
	v_fmac_f32_e32 v134, 0x3dcccccd, v130
	v_fmac_f32_e32 v135, 0x3dcccccd, v134
	v_fma_f32 v130, -v135, v1, v9
	v_fmac_f32_e32 v134, 0x3dcccccd, v130
	v_fmac_f32_e32 v135, 0x3dcccccd, v134
	v_fma_f32 v130, -v135, v1, v10
	v_fmac_f32_e32 v134, 0x3dcccccd, v130
	v_fmac_f32_e32 v135, 0x3dcccccd, v134
	v_fma_f32 v130, -v135, v1, v11
	v_fmac_f32_e32 v134, 0x3dcccccd, v130
	v_fmac_f32_e32 v135, 0x3dcccccd, v134
	v_fma_f32 v130, -v135, v1, v12
	v_fmac_f32_e32 v134, 0x3dcccccd, v130
	v_fmac_f32_e32 v135, 0x3dcccccd, v134
	v_fma_f32 v130, -v135, v1, v13
	v_fmac_f32_e32 v134, 0x3dcccccd, v130
	v_fmac_f32_e32 v135, 0x3dcccccd, v134
	v_fma_f32 v130, -v135, v1, v14
	v_fmac_f32_e32 v134, 0x3dcccccd, v130
	v_fmac_f32_e32 v135, 0x3dcccccd, v134
	v_fma_f32 v130, -v135, v1, v15
	v_fmac_f32_e32 v134, 0x3dcccccd, v130
	v_fmac_f32_e32 v135, 0x3dcccccd, v134
	v_fma_f32 v130, -v135, v1, v16
	v_fmac_f32_e32 v134, 0x3dcccccd, v130
	v_fmac_f32_e32 v135, 0x3dcccccd, v134
	v_lshlrev_b32_e32 v142, 3, v203
	v_lshlrev_b32_e32 v140, 3, v204
	v_fma_f32 v130, -v135, v1, v17
	v_add3_u32 v150, 0, v142, v140
	v_fmac_f32_e32 v134, 0x3dcccccd, v130
	s_mov_b32 s10, 0xbc23d70b
	v_lshl_add_u32 v0, v202, 12, v150
	v_fmac_f32_e32 v133, 0x3dcccccd, v132
	v_fmac_f32_e32 v135, 0x3dcccccd, v134
	v_fma_f32 v130, v131, s10, 1.0
	ds_write2_b64 v0, v[132:133], v[134:135] offset1:32
	v_pk_mul_f32 v[132:133], v[130:131], s[6:7]
	s_lshl_b64 s[2:3], s[2:3], 13
	v_mov_b32_e32 v132, v130
	v_pk_mul_f32 v[136:137], v[132:133], s[6:7] op_sel_hi:[1,0]
	v_pk_mul_f32 v[138:139], v[130:131], v[132:133] op_sel_hi:[0,1]
	v_add_f32_e32 v0, 1.0, v137
	v_mov_b32_e32 v136, v137
	v_mov_b32_e32 v137, v133
	v_pk_fma_f32 v[144:145], v[130:131], v[132:133], v[136:137] op_sel_hi:[0,1,1]
	v_mov_b32_e32 v136, 0x3dcccccd
	v_mov_b32_e32 v137, v139
	v_pk_fma_f32 v[146:147], v[130:131], s[6:7], v[136:137]
	v_mov_b32_e32 v137, v138
	v_pk_fma_f32 v[132:133], v[132:133], s[6:7], v[136:137] op_sel_hi:[1,0,1]
	v_mov_b32_e32 v152, v144
	v_pk_mul_f32 v[132:133], v[144:145], v[132:133]
	v_mov_b32_e32 v145, v147
	v_mov_b32_e32 v153, v146
	v_mov_b32_e32 v138, v147
	v_mov_b32_e32 v139, v0
	v_mov_b32_e32 v148, v146
	v_mov_b32_e32 v149, v0
	v_pk_mul_f32 v[144:145], v[144:145], v[152:153]
	v_pk_fma_f32 v[132:133], v[0:1], v[146:147], v[132:133] op_sel_hi:[0,1,1]
	v_pk_fma_f32 v[138:139], v[138:139], v[148:149], v[144:145]
	s_add_u32 s8, s4, s2
	v_pk_mul_f32 v[144:145], v[132:133], v[138:139] op_sel_hi:[1,0]
	s_waitcnt lgkmcnt(0)
	v_pk_fma_f32 v[144:145], v[138:139], v[132:133], v[144:145] op_sel:[1,0,0]
	v_pk_mul_f32 v[132:133], v[132:133], v[132:133] op_sel:[1,0] op_sel_hi:[1,0]
	s_barrier
	v_pk_fma_f32 v[132:133], v[138:139], v[138:139], v[132:133]
	s_nop 0
	v_pk_mul_f32 v[138:139], v[144:145], v[132:133] op_sel_hi:[1,0]
	s_addc_u32 s3, s5, s3
	v_pk_fma_f32 v[138:139], v[132:133], v[144:145], v[138:139] op_sel:[1,0,0]
	v_pk_mul_f32 v[144:145], v[144:145], v[144:145] op_sel:[1,0] op_sel_hi:[1,0]
	s_lshl_b32 s2, s34, 3
	v_pk_fma_f32 v[132:133], v[132:133], v[132:133], v[144:145]
	ds_read_b64 v[148:149], v150
	v_pk_mul_f32 v[144:145], v[138:139], v[132:133] op_sel_hi:[1,0]
	s_add_u32 s8, s8, s2
	v_pk_fma_f32 v[144:145], v[132:133], v[138:139], v[144:145] op_sel:[1,0,0]
	v_pk_mul_f32 v[138:139], v[138:139], v[138:139] op_sel:[1,0] op_sel_hi:[1,0]
	v_mov_b32_e32 v143, 0
	v_pk_fma_f32 v[132:133], v[132:133], v[132:133], v[138:139]
	s_addc_u32 s9, s3, 0
	v_pk_mul_f32 v[138:139], v[132:133], v[132:133]
	v_pk_mul_f32 v[146:147], v[144:145], v[132:133] op_sel_hi:[1,0]
	v_mov_b32_e32 v141, v143
	v_pk_fma_f32 v[132:133], v[132:133], v[144:145], v[146:147] op_sel:[1,0,0]
	v_pk_fma_f32 v[146:147], v[144:145], v[144:145], v[138:139] op_sel:[1,0,0] op_sel_hi:[1,0,1]
	v_lshl_add_u64 v[138:139], s[8:9], 0, v[142:143]
	v_mov_b32_e32 v135, 1.0
	v_cmp_eq_u32_e64 s[0:1], 0, v202
	v_cmp_ne_u32_e32 vcc, 0, v202
	v_lshl_add_u64 v[144:145], v[138:139], 0, v[140:141]
	s_and_saveexec_b64 s[8:9], vcc
	s_cbranch_execz .LBB1_18
	ds_read_b64 v[138:139], v150 offset:4096
	v_mov_b32_e32 v152, v147
	v_mov_b32_e32 v153, v133
	s_waitcnt lgkmcnt(1)
	v_pk_mul_f32 v[152:153], v[148:149], v[152:153]
	s_nop 0
	v_add_f32_e32 v0, v152, v153
	v_mov_b32_e32 v152, v132
	v_mov_b32_e32 v153, v146
	v_pk_mul_f32 v[152:153], v[148:149], v[152:153]
	s_waitcnt lgkmcnt(0)
	v_add_f32_e32 v0, v138, v0
	v_add_f32_e32 v130, v152, v153
	v_add_f32_e32 v130, v139, v130
	v_or_b32_e32 v139, 1, v130
	v_or_b32_e32 v138, 1, v0
	global_store_dwordx2 v[144:145], v[138:139], off sc1
